# grid barrier: waiters poll the top arrival counter itself (released at (generation+1) x XCC count) instead of a generation word written by the last arriver after its atomic returned; the generation wo
# baseline (speedup 1.0000x reference)
; __device__ __forceinline__ unsigned xb_ld(unsigned* p)              { return __hip_atomic_load(p, __ATOMIC_RELAXED, __HIP_MEMORY_SCOPE_AGENT); }
; __device__ __forceinline__ unsigned xb_add(unsigned* p, unsigned v) { return __hip_atomic_fetch_add(p, v, __ATOMIC_RELAXED, __HIP_MEMORY_SCOPE_AGENT); }
; #define XB_SPIN(cond, bar) do { unsigned _sp = 0; while (cond) { __builtin_amdgcn_s_sleep(1); \
;     if ((++_sp & 255u) == 0u) { if (xb_ld(&(bar)[XB_TMO])) break; if (_sp > XB_SPIN_CAP) { atomicAdd(&(bar)[XB_TMO], 1u); break; } } } } while (0)
; __device__ __forceinline__ void xcd_barrier(const XcdBarrier& b) {
;     ...
;             const unsigned og = xb_add(&bar[XB_TOP], 1u);
;             const unsigned tg = og / nx;
;             if (og + 1u == (tg + 1u) * nx) xb_add(&bar[XB_TOPGEN], 1u);
;             else XB_SPIN(xb_ld(&bar[XB_TOPGEN]) == tg, bar);
.LBB0_129:
	s_or_b64 exec, exec, s[10:11]
	v_cvt_f32_u32_e32 v5, v3
	s_waitcnt vmcnt(0)
	v_readfirstlane_b32 s3, v4
	v_sub_u32_e32 v4, 0, v3
	v_rcp_iflag_f32_e32 v5, v5
	v_add_u32_e32 v6, s3, v2
	v_mul_f32_e32 v5, 0x4f7ffffe, v5
	v_cvt_u32_f32_e32 v5, v5
	v_mul_lo_u32 v2, v4, v5
	v_mul_hi_u32 v2, v5, v2
	v_add_u32_e32 v2, v5, v2
	v_mul_hi_u32 v2, v6, v2
	v_mul_lo_u32 v4, v2, v3
	v_sub_u32_e32 v4, v6, v4
	v_add_u32_e32 v5, 1, v2
	v_cmp_ge_u32_e32 vcc, v4, v3
	s_nop 1
	v_cndmask_b32_e32 v2, v2, v5, vcc
	v_sub_u32_e32 v5, v4, v3
	v_cndmask_b32_e32 v4, v4, v5, vcc
	v_add_u32_e32 v5, 1, v2
	v_cmp_ge_u32_e32 vcc, v4, v3
	v_add_u32_e32 v4, 1, v6
	s_nop 0
	v_cndmask_b32_e32 v2, v2, v5, vcc
	v_mul_lo_u32 v5, v3, v2
	v_add_u32_e32 v3, v5, v3
	v_cmp_ne_u32_e32 vcc, v4, v3
	s_and_saveexec_b64 s[8:9], vcc
	s_xor_b64 s[8:9], exec, s[8:9]
	s_cbranch_execz .LBB0_143
	s_waitcnt lgkmcnt(0)
	v_mad_u32_u24 v2, v1, v2, v1
	s_add_u32 s16, s84, 0x7400
	s_addc_u32 s17, s85, 0
	v_mov_b32_e32 v1, 0
	global_load_dword v1, v1, s[16:17] sc1
	s_waitcnt vmcnt(0)
	v_cmp_gt_u32_e32 vcc, v2, v1
	s_and_saveexec_b64 s[10:11], vcc
	s_cbranch_execz .LBB0_142
	s_add_u32 s14, s84, 0x4200
	s_addc_u32 s15, s85, 0
	s_mov_b32 s3, 1
	s_mov_b64 s[18:19], 0
	v_mov_b32_e32 v1, 0
	s_branch .LBB0_133

; __device__ __forceinline__ unsigned xb_ld(unsigned* p)              { return __hip_atomic_load(p, __ATOMIC_RELAXED, __HIP_MEMORY_SCOPE_AGENT); }
; #define XB_SPIN(cond, bar) do { unsigned _sp = 0; while (cond) { __builtin_amdgcn_s_sleep(1); \
;     if ((++_sp & 255u) == 0u) { if (xb_ld(&(bar)[XB_TMO])) break; if (_sp > XB_SPIN_CAP) { atomicAdd(&(bar)[XB_TMO], 1u); break; } } } } while (0)
; __device__ __forceinline__ void xcd_barrier(const XcdBarrier& b) {
;     ...
;             else XB_SPIN(xb_ld(&bar[XB_TOPGEN]) == tg, bar);
.LBB0_137:
	global_load_dword v3, v1, s[16:17] sc1
	s_add_i32 s3, s3, 1
	s_mov_b64 s[24:25], -1
	s_waitcnt vmcnt(0)
	v_cmp_ge_u32_e32 vcc, v3, v2
	s_orn2_b64 s[22:23], vcc, exec
	s_branch .LBB0_132

; __device__ __forceinline__ unsigned xb_ld(unsigned* p)              { return __hip_atomic_load(p, __ATOMIC_RELAXED, __HIP_MEMORY_SCOPE_AGENT); }
; __device__ __forceinline__ unsigned xb_add(unsigned* p, unsigned v) { return __hip_atomic_fetch_add(p, v, __ATOMIC_RELAXED, __HIP_MEMORY_SCOPE_AGENT); }
; #define XB_SPIN(cond, bar) do { unsigned _sp = 0; while (cond) { __builtin_amdgcn_s_sleep(1); \
;     if ((++_sp & 255u) == 0u) { if (xb_ld(&(bar)[XB_TMO])) break; if (_sp > XB_SPIN_CAP) { atomicAdd(&(bar)[XB_TMO], 1u); break; } } } } while (0)
; __device__ __forceinline__ void xcd_barrier(const XcdBarrier& b) {
;     ...
;             const unsigned og = xb_add(&bar[XB_TOP], 1u);
;             const unsigned tg = og / nx;
;             if (og + 1u == (tg + 1u) * nx) xb_add(&bar[XB_TOPGEN], 1u);
;             else XB_SPIN(xb_ld(&bar[XB_TOPGEN]) == tg, bar);
.LBB0_146:
	s_or_b64 exec, exec, s[10:11]
	v_cvt_f32_u32_e32 v4, v1
	s_waitcnt vmcnt(0)
	v_readfirstlane_b32 s3, v3
	s_add_u32 s10, s84, 0x7400
	s_addc_u32 s11, s85, 0
	v_rcp_iflag_f32_e32 v4, v4
	v_add_u32_e32 v2, s3, v2
	v_add_u32_e32 v5, 1, v2
	s_mov_b64 s[14:15], -1
	v_mul_f32_e32 v3, 0x4f7ffffe, v4
	v_cvt_u32_f32_e32 v3, v3
	v_sub_u32_e32 v4, 0, v1
	v_mul_lo_u32 v4, v4, v3
	v_mul_hi_u32 v4, v3, v4
	v_add_u32_e32 v3, v3, v4
	v_mul_hi_u32 v3, v2, v3
	v_mul_lo_u32 v4, v3, v1
	v_sub_u32_e32 v2, v2, v4
	v_add_u32_e32 v6, 1, v3
	v_cmp_ge_u32_e32 vcc, v2, v1
	v_sub_u32_e32 v4, v2, v1
	s_nop 0
	v_cndmask_b32_e32 v3, v3, v6, vcc
	v_cndmask_b32_e32 v2, v2, v4, vcc
	v_add_u32_e32 v4, 1, v3
	v_cmp_ge_u32_e32 vcc, v2, v1
	s_nop 1
	v_cndmask_b32_e32 v4, v3, v4, vcc
	v_mul_lo_u32 v2, v1, v4
	v_add_u32_e32 v1, v2, v1
	v_cmp_ne_u32_e32 vcc, v5, v1
	v_mov_b32_e32 v4, v1
	v_mov_b64_e32 v[2:3], s[10:11]
	s_and_saveexec_b64 s[8:9], vcc
	s_cbranch_execz .LBB0_158
	v_mov_b32_e32 v1, 0
	global_load_dword v2, v1, s[10:11] sc1
	s_mov_b64 s[18:19], 0
	s_waitcnt vmcnt(0)
	v_cmp_gt_u32_e32 vcc, v4, v2
	s_and_saveexec_b64 s[16:17], vcc
	s_cbranch_execz .LBB0_157
	s_add_u32 s14, s84, 0x4200
	s_addc_u32 s15, s85, 0
	s_mov_b32 s3, 1
	s_branch .LBB0_150

; __device__ __forceinline__ unsigned xb_ld(unsigned* p)              { return __hip_atomic_load(p, __ATOMIC_RELAXED, __HIP_MEMORY_SCOPE_AGENT); }
; #define XB_SPIN(cond, bar) do { unsigned _sp = 0; while (cond) { __builtin_amdgcn_s_sleep(1); \
;     if ((++_sp & 255u) == 0u) { if (xb_ld(&(bar)[XB_TMO])) break; if (_sp > XB_SPIN_CAP) { atomicAdd(&(bar)[XB_TMO], 1u); break; } } } } while (0)
; __device__ __forceinline__ void xcd_barrier(const XcdBarrier& b) {
;     ...
;             else XB_SPIN(xb_ld(&bar[XB_TOPGEN]) == tg, bar);
.LBB0_154:
	global_load_dword v2, v1, s[10:11] sc1
	s_add_i32 s3, s3, 1
	s_mov_b64 s[22:23], -1
	s_waitcnt vmcnt(0)
	v_cmp_ge_u32_e32 vcc, v2, v4
	s_orn2_b64 s[26:27], vcc, exec
	s_branch .LBB0_149

; __device__ __forceinline__ unsigned xb_ld(unsigned* p)              { return __hip_atomic_load(p, __ATOMIC_RELAXED, __HIP_MEMORY_SCOPE_AGENT); }
; __device__ __forceinline__ unsigned xb_add(unsigned* p, unsigned v) { return __hip_atomic_fetch_add(p, v, __ATOMIC_RELAXED, __HIP_MEMORY_SCOPE_AGENT); }
; #define XB_SPIN(cond, bar) do { unsigned _sp = 0; while (cond) { __builtin_amdgcn_s_sleep(1); \
;     if ((++_sp & 255u) == 0u) { if (xb_ld(&(bar)[XB_TMO])) break; if (_sp > XB_SPIN_CAP) { atomicAdd(&(bar)[XB_TMO], 1u); break; } } } } while (0)
; __device__ __forceinline__ void xcd_barrier(const XcdBarrier& b) {
;     ...
;             if (og + 1u == (tg + 1u) * nx) xb_add(&bar[XB_TOPGEN], 1u);
;             else XB_SPIN(xb_ld(&bar[XB_TOPGEN]) == tg, bar);
;             __builtin_amdgcn_fence(__ATOMIC_ACQUIRE, "agent");
;             xb_add(&bar[XB_XGEN(b.x)], 1u);
.LBB0_158:
	s_or_b64 exec, exec, s[8:9]
	s_and_saveexec_b64 s[8:9], s[14:15]
	s_cbranch_execz .LBB0_160
	v_mov_b32_e32 v1, 1
.LBB0_160:
	s_or_b64 exec, exec, s[8:9]
	s_mov_b64 s[8:9], exec
	v_mbcnt_lo_u32_b32 v1, s8, 0
	v_mbcnt_hi_u32_b32 v1, s9, v1
	v_cmp_eq_u32_e32 vcc, 0, v1
	s_waitcnt vmcnt(0)
	buffer_inv sc1
	s_and_saveexec_b64 s[10:11], vcc
	s_cbranch_execz .LBB0_162
	s_bcnt1_i32_b64 s3, s[8:9]
	v_mov_b32_e32 v1, 0x2000
	v_mov_b32_e32 v2, s3

; __device__ __forceinline__ unsigned xb_ld(unsigned* p)              { return __hip_atomic_load(p, __ATOMIC_RELAXED, __HIP_MEMORY_SCOPE_AGENT); }
; __device__ __forceinline__ unsigned xb_add(unsigned* p, unsigned v) { return __hip_atomic_fetch_add(p, v, __ATOMIC_RELAXED, __HIP_MEMORY_SCOPE_AGENT); }
; #define XB_SPIN(cond, bar) do { unsigned _sp = 0; while (cond) { __builtin_amdgcn_s_sleep(1); \
;     if ((++_sp & 255u) == 0u) { if (xb_ld(&(bar)[XB_TMO])) break; if (_sp > XB_SPIN_CAP) { atomicAdd(&(bar)[XB_TMO], 1u); break; } } } } while (0)
; __device__ __forceinline__ void xcd_barrier(const XcdBarrier& b) {
;     ...
;             const unsigned og = xb_add(&bar[XB_TOP], 1u);
;             const unsigned tg = og / nx;
;             if (og + 1u == (tg + 1u) * nx) xb_add(&bar[XB_TOPGEN], 1u);
;             else XB_SPIN(xb_ld(&bar[XB_TOPGEN]) == tg, bar);
.LBB0_281:
	s_or_b64 exec, exec, s[10:11]
	v_cvt_f32_u32_e32 v5, v3
	s_waitcnt vmcnt(0)
	v_readfirstlane_b32 s3, v4
	v_sub_u32_e32 v4, 0, v3
	v_rcp_iflag_f32_e32 v5, v5
	v_add_u32_e32 v6, s3, v2
	v_mul_f32_e32 v5, 0x4f7ffffe, v5
	v_cvt_u32_f32_e32 v5, v5
	v_mul_lo_u32 v2, v4, v5
	v_mul_hi_u32 v2, v5, v2
	v_add_u32_e32 v2, v5, v2
	v_mul_hi_u32 v2, v6, v2
	v_mul_lo_u32 v4, v2, v3
	v_sub_u32_e32 v4, v6, v4
	v_add_u32_e32 v5, 1, v2
	v_cmp_ge_u32_e32 vcc, v4, v3
	s_nop 1
	v_cndmask_b32_e32 v2, v2, v5, vcc
	v_sub_u32_e32 v5, v4, v3
	v_cndmask_b32_e32 v4, v4, v5, vcc
	v_add_u32_e32 v5, 1, v2
	v_cmp_ge_u32_e32 vcc, v4, v3
	v_add_u32_e32 v4, 1, v6
	s_nop 0
	v_cndmask_b32_e32 v2, v2, v5, vcc
	v_mul_lo_u32 v5, v3, v2
	v_add_u32_e32 v3, v5, v3
	v_cmp_ne_u32_e32 vcc, v4, v3
	s_and_saveexec_b64 s[8:9], vcc
	s_xor_b64 s[8:9], exec, s[8:9]
	s_cbranch_execz .LBB0_295
	s_waitcnt lgkmcnt(0)
	v_mad_u32_u24 v2, v1, v2, v1
	s_add_u32 s16, s84, 0x7400
	s_addc_u32 s17, s85, 0
	v_mov_b32_e32 v1, 0
	global_load_dword v1, v1, s[16:17] sc1
	s_waitcnt vmcnt(0)
	v_cmp_gt_u32_e32 vcc, v2, v1
	s_and_saveexec_b64 s[10:11], vcc
	s_cbranch_execz .LBB0_294
	s_add_u32 s14, s84, 0x4200
	s_addc_u32 s15, s85, 0
	s_mov_b32 s3, 1
	s_mov_b64 s[18:19], 0
	s_branch .LBB0_285

; __device__ __forceinline__ unsigned xb_ld(unsigned* p)              { return __hip_atomic_load(p, __ATOMIC_RELAXED, __HIP_MEMORY_SCOPE_AGENT); }
; #define XB_SPIN(cond, bar) do { unsigned _sp = 0; while (cond) { __builtin_amdgcn_s_sleep(1); \
;     if ((++_sp & 255u) == 0u) { if (xb_ld(&(bar)[XB_TMO])) break; if (_sp > XB_SPIN_CAP) { atomicAdd(&(bar)[XB_TMO], 1u); break; } } } } while (0)
; __device__ __forceinline__ void xcd_barrier(const XcdBarrier& b) {
;     ...
;             else XB_SPIN(xb_ld(&bar[XB_TOPGEN]) == tg, bar);
.LBB0_289:
	global_load_dword v1, v195, s[16:17] sc1
	s_add_i32 s3, s3, 1
	s_mov_b64 s[24:25], -1
	s_waitcnt vmcnt(0)
	v_cmp_ge_u32_e32 vcc, v1, v2
	s_orn2_b64 s[22:23], vcc, exec
	s_branch .LBB0_284

; __device__ __forceinline__ unsigned xb_ld(unsigned* p)              { return __hip_atomic_load(p, __ATOMIC_RELAXED, __HIP_MEMORY_SCOPE_AGENT); }
; __device__ __forceinline__ unsigned xb_add(unsigned* p, unsigned v) { return __hip_atomic_fetch_add(p, v, __ATOMIC_RELAXED, __HIP_MEMORY_SCOPE_AGENT); }
; #define XB_SPIN(cond, bar) do { unsigned _sp = 0; while (cond) { __builtin_amdgcn_s_sleep(1); \
;     if ((++_sp & 255u) == 0u) { if (xb_ld(&(bar)[XB_TMO])) break; if (_sp > XB_SPIN_CAP) { atomicAdd(&(bar)[XB_TMO], 1u); break; } } } } while (0)
; __device__ __forceinline__ void xcd_barrier(const XcdBarrier& b) {
;     ...
;             const unsigned og = xb_add(&bar[XB_TOP], 1u);
;             const unsigned tg = og / nx;
;             if (og + 1u == (tg + 1u) * nx) xb_add(&bar[XB_TOPGEN], 1u);
;             else XB_SPIN(xb_ld(&bar[XB_TOPGEN]) == tg, bar);
.LBB0_298:
	s_or_b64 exec, exec, s[10:11]
	v_cvt_f32_u32_e32 v4, v1
	s_waitcnt vmcnt(0)
	v_readfirstlane_b32 s3, v3
	s_add_u32 s8, s84, 0x7400
	s_addc_u32 s9, s85, 0
	v_rcp_iflag_f32_e32 v4, v4
	v_add_u32_e32 v2, s3, v2
	v_add_u32_e32 v5, 1, v2
	s_mov_b64 s[14:15], -1
	v_mul_f32_e32 v3, 0x4f7ffffe, v4
	v_cvt_u32_f32_e32 v3, v3
	v_sub_u32_e32 v4, 0, v1
	v_mul_lo_u32 v4, v4, v3
	v_mul_hi_u32 v4, v3, v4
	v_add_u32_e32 v3, v3, v4
	v_mul_hi_u32 v3, v2, v3
	v_mul_lo_u32 v4, v3, v1
	v_sub_u32_e32 v2, v2, v4
	v_add_u32_e32 v6, 1, v3
	v_cmp_ge_u32_e32 vcc, v2, v1
	v_sub_u32_e32 v4, v2, v1
	s_nop 0
	v_cndmask_b32_e32 v3, v3, v6, vcc
	v_cndmask_b32_e32 v2, v2, v4, vcc
	v_add_u32_e32 v4, 1, v3
	v_cmp_ge_u32_e32 vcc, v2, v1
	s_nop 1
	v_cndmask_b32_e32 v4, v3, v4, vcc
	v_mul_lo_u32 v2, v1, v4
	v_add_u32_e32 v1, v2, v1
	v_cmp_ne_u32_e32 vcc, v5, v1
	v_mov_b32_e32 v4, v1
	v_mov_b64_e32 v[2:3], s[8:9]
	s_and_saveexec_b64 s[10:11], vcc
	s_cbranch_execz .LBB0_310
	global_load_dword v1, v195, s[8:9] sc1
	s_mov_b64 s[18:19], 0
	s_waitcnt vmcnt(0)
	v_cmp_gt_u32_e32 vcc, v4, v1
	s_and_saveexec_b64 s[16:17], vcc
	s_cbranch_execz .LBB0_309
	s_add_u32 s14, s84, 0x4200
	s_addc_u32 s15, s85, 0
	s_mov_b32 s3, 1
	s_branch .LBB0_302

; __device__ __forceinline__ unsigned xb_ld(unsigned* p)              { return __hip_atomic_load(p, __ATOMIC_RELAXED, __HIP_MEMORY_SCOPE_AGENT); }
; #define XB_SPIN(cond, bar) do { unsigned _sp = 0; while (cond) { __builtin_amdgcn_s_sleep(1); \
;     if ((++_sp & 255u) == 0u) { if (xb_ld(&(bar)[XB_TMO])) break; if (_sp > XB_SPIN_CAP) { atomicAdd(&(bar)[XB_TMO], 1u); break; } } } } while (0)
; __device__ __forceinline__ void xcd_barrier(const XcdBarrier& b) {
;     ...
;             else XB_SPIN(xb_ld(&bar[XB_TOPGEN]) == tg, bar);
.LBB0_306:
	global_load_dword v1, v195, s[8:9] sc1
	s_add_i32 s3, s3, 1
	s_mov_b64 s[24:25], -1
	s_waitcnt vmcnt(0)
	v_cmp_ge_u32_e32 vcc, v1, v4
	s_orn2_b64 s[22:23], vcc, exec
	s_branch .LBB0_301

; __device__ __forceinline__ unsigned xb_ld(unsigned* p)              { return __hip_atomic_load(p, __ATOMIC_RELAXED, __HIP_MEMORY_SCOPE_AGENT); }
; __device__ __forceinline__ unsigned xb_add(unsigned* p, unsigned v) { return __hip_atomic_fetch_add(p, v, __ATOMIC_RELAXED, __HIP_MEMORY_SCOPE_AGENT); }
; #define XB_SPIN(cond, bar) do { unsigned _sp = 0; while (cond) { __builtin_amdgcn_s_sleep(1); \
;     if ((++_sp & 255u) == 0u) { if (xb_ld(&(bar)[XB_TMO])) break; if (_sp > XB_SPIN_CAP) { atomicAdd(&(bar)[XB_TMO], 1u); break; } } } } while (0)
; __device__ __forceinline__ void xcd_barrier(const XcdBarrier& b) {
;     ...
;             if (og + 1u == (tg + 1u) * nx) xb_add(&bar[XB_TOPGEN], 1u);
;             else XB_SPIN(xb_ld(&bar[XB_TOPGEN]) == tg, bar);
;             __builtin_amdgcn_fence(__ATOMIC_ACQUIRE, "agent");
;             xb_add(&bar[XB_XGEN(b.x)], 1u);
.LBB0_310:
	s_or_b64 exec, exec, s[10:11]
	s_and_saveexec_b64 s[8:9], s[14:15]
	s_cbranch_execz .LBB0_312
.LBB0_312:
	s_or_b64 exec, exec, s[8:9]
	s_mov_b64 s[8:9], exec
	v_mbcnt_lo_u32_b32 v1, s8, 0
	v_mbcnt_hi_u32_b32 v1, s9, v1
	v_cmp_eq_u32_e32 vcc, 0, v1
	s_waitcnt vmcnt(0)
	buffer_inv sc1
	s_and_saveexec_b64 s[10:11], vcc
	s_cbranch_execz .LBB0_314
	s_bcnt1_i32_b64 s3, s[8:9]
	v_mov_b32_e32 v1, s3
	v_mov_b32_e32 v2, 0x2000

; __device__ __forceinline__ unsigned xb_ld(unsigned* p)              { return __hip_atomic_load(p, __ATOMIC_RELAXED, __HIP_MEMORY_SCOPE_AGENT); }
; __device__ __forceinline__ unsigned xb_add(unsigned* p, unsigned v) { return __hip_atomic_fetch_add(p, v, __ATOMIC_RELAXED, __HIP_MEMORY_SCOPE_AGENT); }
; #define XB_SPIN(cond, bar) do { unsigned _sp = 0; while (cond) { __builtin_amdgcn_s_sleep(1); \
;     if ((++_sp & 255u) == 0u) { if (xb_ld(&(bar)[XB_TMO])) break; if (_sp > XB_SPIN_CAP) { atomicAdd(&(bar)[XB_TMO], 1u); break; } } } } while (0)
; __device__ __forceinline__ void xcd_barrier(const XcdBarrier& b) {
;     ...
;             const unsigned og = xb_add(&bar[XB_TOP], 1u);
;             const unsigned tg = og / nx;
;             if (og + 1u == (tg + 1u) * nx) xb_add(&bar[XB_TOPGEN], 1u);
;             else XB_SPIN(xb_ld(&bar[XB_TOPGEN]) == tg, bar);
.LBB0_351:
	s_or_b64 exec, exec, s[10:11]
	v_cvt_f32_u32_e32 v5, v3
	s_waitcnt vmcnt(0)
	v_readfirstlane_b32 s3, v4
	v_sub_u32_e32 v4, 0, v3
	v_rcp_iflag_f32_e32 v5, v5
	v_add_u32_e32 v6, s3, v1
	v_mul_f32_e32 v5, 0x4f7ffffe, v5
	v_cvt_u32_f32_e32 v5, v5
	v_mul_lo_u32 v1, v4, v5
	v_mul_hi_u32 v1, v5, v1
	v_add_u32_e32 v1, v5, v1
	v_mul_hi_u32 v1, v6, v1
	v_mul_lo_u32 v4, v1, v3
	v_sub_u32_e32 v4, v6, v4
	v_add_u32_e32 v5, 1, v1
	v_cmp_ge_u32_e32 vcc, v4, v3
	s_nop 1
	v_cndmask_b32_e32 v1, v1, v5, vcc
	v_sub_u32_e32 v5, v4, v3
	v_cndmask_b32_e32 v4, v4, v5, vcc
	v_add_u32_e32 v5, 1, v1
	v_cmp_ge_u32_e32 vcc, v4, v3
	v_add_u32_e32 v4, 1, v6
	s_nop 0
	v_cndmask_b32_e32 v1, v1, v5, vcc
	v_mul_lo_u32 v5, v3, v1
	v_add_u32_e32 v3, v5, v3
	v_cmp_ne_u32_e32 vcc, v4, v3
	s_and_saveexec_b64 s[8:9], vcc
	s_xor_b64 s[8:9], exec, s[8:9]
	s_cbranch_execz .LBB0_365
	s_waitcnt lgkmcnt(0)
	v_mad_u32_u24 v1, v2, v1, v2
	s_add_u32 s20, s34, 0x7400
	s_addc_u32 s21, s35, 0
	v_mov_b32_e32 v2, 0
	global_load_dword v2, v2, s[20:21] sc1
	s_waitcnt vmcnt(0)
	v_cmp_gt_u32_e32 vcc, v1, v2
	s_and_saveexec_b64 s[10:11], vcc
	s_cbranch_execz .LBB0_364
	s_add_u32 s14, s34, 0x4200
	s_addc_u32 s15, s35, 0
	s_mov_b32 s3, 1
	s_mov_b64 s[22:23], 0
	s_branch .LBB0_355

; __device__ __forceinline__ unsigned xb_ld(unsigned* p)              { return __hip_atomic_load(p, __ATOMIC_RELAXED, __HIP_MEMORY_SCOPE_AGENT); }
; #define XB_SPIN(cond, bar) do { unsigned _sp = 0; while (cond) { __builtin_amdgcn_s_sleep(1); \
;     if ((++_sp & 255u) == 0u) { if (xb_ld(&(bar)[XB_TMO])) break; if (_sp > XB_SPIN_CAP) { atomicAdd(&(bar)[XB_TMO], 1u); break; } } } } while (0)
; __device__ __forceinline__ void xcd_barrier(const XcdBarrier& b) {
;     ...
;             else XB_SPIN(xb_ld(&bar[XB_TOPGEN]) == tg, bar);
.LBB0_359:
	global_load_dword v2, v195, s[20:21] sc1
	s_add_i32 s3, s3, 1
	s_mov_b64 s[28:29], -1
	s_waitcnt vmcnt(0)
	v_cmp_ge_u32_e32 vcc, v2, v1
	s_orn2_b64 s[24:25], vcc, exec
	s_branch .LBB0_354

; __device__ __forceinline__ unsigned xb_ld(unsigned* p)              { return __hip_atomic_load(p, __ATOMIC_RELAXED, __HIP_MEMORY_SCOPE_AGENT); }
; __device__ __forceinline__ unsigned xb_add(unsigned* p, unsigned v) { return __hip_atomic_fetch_add(p, v, __ATOMIC_RELAXED, __HIP_MEMORY_SCOPE_AGENT); }
; #define XB_SPIN(cond, bar) do { unsigned _sp = 0; while (cond) { __builtin_amdgcn_s_sleep(1); \
;     if ((++_sp & 255u) == 0u) { if (xb_ld(&(bar)[XB_TMO])) break; if (_sp > XB_SPIN_CAP) { atomicAdd(&(bar)[XB_TMO], 1u); break; } } } } while (0)
; __device__ __forceinline__ void xcd_barrier(const XcdBarrier& b) {
;     ...
;             const unsigned og = xb_add(&bar[XB_TOP], 1u);
;             const unsigned tg = og / nx;
;             if (og + 1u == (tg + 1u) * nx) xb_add(&bar[XB_TOPGEN], 1u);
;             else XB_SPIN(xb_ld(&bar[XB_TOPGEN]) == tg, bar);
.LBB0_368:
	s_or_b64 exec, exec, s[10:11]
	s_waitcnt vmcnt(0)
	v_readfirstlane_b32 s3, v3
	v_sub_u32_e32 v4, 0, v2
	s_add_u32 s8, s34, 0x7400
	v_add_u32_e32 v3, s3, v1
	v_cvt_f32_u32_e32 v1, v2
	s_addc_u32 s9, s35, 0
	s_mov_b64 s[14:15], -1
	v_rcp_iflag_f32_e32 v1, v1
	s_nop 0
	v_mul_f32_e32 v1, 0x4f7ffffe, v1
	v_cvt_u32_f32_e32 v1, v1
	v_mul_lo_u32 v4, v4, v1
	v_mul_hi_u32 v4, v1, v4
	v_add_u32_e32 v1, v1, v4
	v_mul_hi_u32 v1, v3, v1
	v_mul_lo_u32 v4, v1, v2
	v_sub_u32_e32 v4, v3, v4
	v_cmp_ge_u32_e32 vcc, v4, v2
	v_add_u32_e32 v5, 1, v1
	v_add_u32_e32 v3, 1, v3
	v_cndmask_b32_e32 v1, v1, v5, vcc
	v_sub_u32_e32 v5, v4, v2
	v_cndmask_b32_e32 v4, v4, v5, vcc
	v_cmp_ge_u32_e32 vcc, v4, v2
	v_add_u32_e32 v4, 1, v1
	s_nop 0
	v_cndmask_b32_e32 v1, v1, v4, vcc
	v_mul_lo_u32 v4, v2, v1
	v_add_u32_e32 v2, v4, v2
	v_cmp_ne_u32_e32 vcc, v3, v2
	v_mov_b32_e32 v1, v2
	v_mov_b64_e32 v[2:3], s[8:9]
	s_and_saveexec_b64 s[10:11], vcc
	s_cbranch_execz .LBB0_380
	global_load_dword v2, v195, s[8:9] sc1
	s_mov_b64 s[22:23], 0
	s_waitcnt vmcnt(0)
	v_cmp_gt_u32_e32 vcc, v1, v2
	s_and_saveexec_b64 s[20:21], vcc
	s_cbranch_execz .LBB0_379
	s_add_u32 s14, s34, 0x4200
	s_addc_u32 s15, s35, 0
	s_mov_b32 s3, 1
	s_branch .LBB0_372

; __device__ __forceinline__ unsigned xb_ld(unsigned* p)              { return __hip_atomic_load(p, __ATOMIC_RELAXED, __HIP_MEMORY_SCOPE_AGENT); }
; #define XB_SPIN(cond, bar) do { unsigned _sp = 0; while (cond) { __builtin_amdgcn_s_sleep(1); \
;     if ((++_sp & 255u) == 0u) { if (xb_ld(&(bar)[XB_TMO])) break; if (_sp > XB_SPIN_CAP) { atomicAdd(&(bar)[XB_TMO], 1u); break; } } } } while (0)
; __device__ __forceinline__ void xcd_barrier(const XcdBarrier& b) {
;     ...
;             else XB_SPIN(xb_ld(&bar[XB_TOPGEN]) == tg, bar);
.LBB0_376:
	global_load_dword v2, v195, s[8:9] sc1
	s_add_i32 s3, s3, 1
	s_mov_b64 s[28:29], -1
	s_waitcnt vmcnt(0)
	v_cmp_ge_u32_e32 vcc, v2, v1
	s_orn2_b64 s[24:25], vcc, exec
	s_branch .LBB0_371

; __device__ __forceinline__ unsigned xb_ld(unsigned* p)              { return __hip_atomic_load(p, __ATOMIC_RELAXED, __HIP_MEMORY_SCOPE_AGENT); }
; __device__ __forceinline__ unsigned xb_add(unsigned* p, unsigned v) { return __hip_atomic_fetch_add(p, v, __ATOMIC_RELAXED, __HIP_MEMORY_SCOPE_AGENT); }
; #define XB_SPIN(cond, bar) do { unsigned _sp = 0; while (cond) { __builtin_amdgcn_s_sleep(1); \
;     if ((++_sp & 255u) == 0u) { if (xb_ld(&(bar)[XB_TMO])) break; if (_sp > XB_SPIN_CAP) { atomicAdd(&(bar)[XB_TMO], 1u); break; } } } } while (0)
; __device__ __forceinline__ void xcd_barrier(const XcdBarrier& b) {
;     ...
;             if (og + 1u == (tg + 1u) * nx) xb_add(&bar[XB_TOPGEN], 1u);
;             else XB_SPIN(xb_ld(&bar[XB_TOPGEN]) == tg, bar);
;             __builtin_amdgcn_fence(__ATOMIC_ACQUIRE, "agent");
;             xb_add(&bar[XB_XGEN(b.x)], 1u);
.LBB0_380:
	s_or_b64 exec, exec, s[10:11]
	s_and_saveexec_b64 s[8:9], s[14:15]
	s_cbranch_execz .LBB0_382
.LBB0_382:
	s_or_b64 exec, exec, s[8:9]
	s_mov_b64 s[8:9], exec
	v_mbcnt_lo_u32_b32 v1, s8, 0
	v_mbcnt_hi_u32_b32 v1, s9, v1
	v_cmp_eq_u32_e32 vcc, 0, v1
	s_waitcnt vmcnt(0)
	buffer_inv sc1
	s_and_saveexec_b64 s[10:11], vcc
	s_cbranch_execz .LBB0_384
	s_bcnt1_i32_b64 s3, s[8:9]
	v_mov_b32_e32 v1, s3
	v_mov_b32_e32 v2, 0x2000

; __device__ __forceinline__ unsigned xb_ld(unsigned* p)              { return __hip_atomic_load(p, __ATOMIC_RELAXED, __HIP_MEMORY_SCOPE_AGENT); }
; __device__ __forceinline__ unsigned xb_add(unsigned* p, unsigned v) { return __hip_atomic_fetch_add(p, v, __ATOMIC_RELAXED, __HIP_MEMORY_SCOPE_AGENT); }
; #define XB_SPIN(cond, bar) do { unsigned _sp = 0; while (cond) { __builtin_amdgcn_s_sleep(1); \
;     if ((++_sp & 255u) == 0u) { if (xb_ld(&(bar)[XB_TMO])) break; if (_sp > XB_SPIN_CAP) { atomicAdd(&(bar)[XB_TMO], 1u); break; } } } } while (0)
; __device__ __forceinline__ void xcd_barrier(const XcdBarrier& b) {
;     ...
;             const unsigned og = xb_add(&bar[XB_TOP], 1u);
;             const unsigned tg = og / nx;
;             if (og + 1u == (tg + 1u) * nx) xb_add(&bar[XB_TOPGEN], 1u);
;             else XB_SPIN(xb_ld(&bar[XB_TOPGEN]) == tg, bar);
.LBB0_436:
	s_or_b64 exec, exec, s[10:11]
	v_cvt_f32_u32_e32 v6, v4
	s_waitcnt vmcnt(0)
	v_readfirstlane_b32 s8, v5
	v_sub_u32_e32 v5, 0, v4
	v_rcp_iflag_f32_e32 v6, v6
	v_add_u32_e32 v7, s8, v3
	v_mul_f32_e32 v6, 0x4f7ffffe, v6
	v_cvt_u32_f32_e32 v6, v6
	v_mul_lo_u32 v3, v5, v6
	v_mul_hi_u32 v3, v6, v3
	v_add_u32_e32 v3, v6, v3
	v_mul_hi_u32 v3, v7, v3
	v_mul_lo_u32 v5, v3, v4
	v_sub_u32_e32 v5, v7, v5
	v_add_u32_e32 v6, 1, v3
	v_cmp_ge_u32_e32 vcc, v5, v4
	s_nop 1
	v_cndmask_b32_e32 v3, v3, v6, vcc
	v_sub_u32_e32 v6, v5, v4
	v_cndmask_b32_e32 v5, v5, v6, vcc
	v_add_u32_e32 v6, 1, v3
	v_cmp_ge_u32_e32 vcc, v5, v4
	v_add_u32_e32 v5, 1, v7
	s_nop 0
	v_cndmask_b32_e32 v3, v3, v6, vcc
	v_mul_lo_u32 v6, v4, v3
	v_add_u32_e32 v4, v6, v4
	v_cmp_ne_u32_e32 vcc, v5, v4
	s_and_saveexec_b64 s[8:9], vcc
	s_xor_b64 s[8:9], exec, s[8:9]
	s_cbranch_execz .LBB0_450
	s_waitcnt lgkmcnt(0)
	v_mad_u32_u24 v3, v2, v3, v2
	s_add_u32 s22, s34, 0x7400
	s_addc_u32 s23, s35, 0
	v_mov_b32_e32 v2, 0
	global_load_dword v2, v2, s[22:23] sc1
	s_waitcnt vmcnt(0)
	v_cmp_gt_u32_e32 vcc, v3, v2
	s_and_saveexec_b64 s[10:11], vcc
	s_cbranch_execz .LBB0_449
	s_add_u32 s14, s34, 0x4200
	s_addc_u32 s15, s35, 0
	s_mov_b32 s16, 1
	s_mov_b64 s[26:27], 0
	s_branch .LBB0_440

; __device__ __forceinline__ unsigned xb_ld(unsigned* p)              { return __hip_atomic_load(p, __ATOMIC_RELAXED, __HIP_MEMORY_SCOPE_AGENT); }
; #define XB_SPIN(cond, bar) do { unsigned _sp = 0; while (cond) { __builtin_amdgcn_s_sleep(1); \
;     if ((++_sp & 255u) == 0u) { if (xb_ld(&(bar)[XB_TMO])) break; if (_sp > XB_SPIN_CAP) { atomicAdd(&(bar)[XB_TMO], 1u); break; } } } } while (0)
; __device__ __forceinline__ void xcd_barrier(const XcdBarrier& b) {
;     ...
;             else XB_SPIN(xb_ld(&bar[XB_TOPGEN]) == tg, bar);
.LBB0_444:
	global_load_dword v2, v195, s[22:23] sc1
	s_add_i32 s16, s16, 1
	s_mov_b64 s[30:31], -1
	s_waitcnt vmcnt(0)
	v_cmp_ge_u32_e32 vcc, v2, v3
	s_orn2_b64 s[24:25], vcc, exec
	s_branch .LBB0_439

; __device__ __forceinline__ unsigned xb_ld(unsigned* p)              { return __hip_atomic_load(p, __ATOMIC_RELAXED, __HIP_MEMORY_SCOPE_AGENT); }
; __device__ __forceinline__ unsigned xb_add(unsigned* p, unsigned v) { return __hip_atomic_fetch_add(p, v, __ATOMIC_RELAXED, __HIP_MEMORY_SCOPE_AGENT); }
; #define XB_SPIN(cond, bar) do { unsigned _sp = 0; while (cond) { __builtin_amdgcn_s_sleep(1); \
;     if ((++_sp & 255u) == 0u) { if (xb_ld(&(bar)[XB_TMO])) break; if (_sp > XB_SPIN_CAP) { atomicAdd(&(bar)[XB_TMO], 1u); break; } } } } while (0)
; __device__ __forceinline__ void xcd_barrier(const XcdBarrier& b) {
;     ...
;             const unsigned og = xb_add(&bar[XB_TOP], 1u);
;             const unsigned tg = og / nx;
;             if (og + 1u == (tg + 1u) * nx) xb_add(&bar[XB_TOPGEN], 1u);
;             else XB_SPIN(xb_ld(&bar[XB_TOPGEN]) == tg, bar);
.LBB0_453:
	s_or_b64 exec, exec, s[10:11]
	s_waitcnt vmcnt(0)
	v_readfirstlane_b32 s8, v4
	v_cvt_f32_u32_e32 v4, v2
	v_sub_u32_e32 v5, 0, v2
	v_add_u32_e32 v3, s8, v3
	s_add_u32 s8, s34, 0x7400
	v_rcp_iflag_f32_e32 v4, v4
	s_addc_u32 s9, s35, 0
	s_mov_b64 s[14:15], -1
	v_mul_f32_e32 v4, 0x4f7ffffe, v4
	v_cvt_u32_f32_e32 v4, v4
	v_mul_lo_u32 v5, v5, v4
	v_mul_hi_u32 v5, v4, v5
	v_add_u32_e32 v4, v4, v5
	v_mul_hi_u32 v4, v3, v4
	v_mul_lo_u32 v5, v4, v2
	v_sub_u32_e32 v5, v3, v5
	v_cmp_ge_u32_e32 vcc, v5, v2
	v_add_u32_e32 v6, 1, v4
	v_add_u32_e32 v3, 1, v3
	v_cndmask_b32_e32 v4, v4, v6, vcc
	v_sub_u32_e32 v6, v5, v2
	v_cndmask_b32_e32 v5, v5, v6, vcc
	v_cmp_ge_u32_e32 vcc, v5, v2
	v_add_u32_e32 v5, 1, v4
	s_nop 0
	v_cndmask_b32_e32 v4, v4, v5, vcc
	v_mul_lo_u32 v5, v2, v4
	v_add_u32_e32 v2, v5, v2
	v_cmp_ne_u32_e32 vcc, v3, v2
	v_mov_b32_e32 v4, v2
	v_mov_b64_e32 v[2:3], s[8:9]
	s_and_saveexec_b64 s[10:11], vcc
	s_cbranch_execz .LBB0_465
	global_load_dword v2, v195, s[8:9] sc1
	s_mov_b64 s[24:25], 0
	s_waitcnt vmcnt(0)
	v_cmp_gt_u32_e32 vcc, v4, v2
	s_and_saveexec_b64 s[22:23], vcc
	s_cbranch_execz .LBB0_464
	s_add_u32 s14, s34, 0x4200
	s_addc_u32 s15, s35, 0
	s_mov_b32 s16, 1
	s_mov_b64 s[26:27], 0
	s_branch .LBB0_457

; __device__ __forceinline__ unsigned xb_ld(unsigned* p)              { return __hip_atomic_load(p, __ATOMIC_RELAXED, __HIP_MEMORY_SCOPE_AGENT); }
; #define XB_SPIN(cond, bar) do { unsigned _sp = 0; while (cond) { __builtin_amdgcn_s_sleep(1); \
;     if ((++_sp & 255u) == 0u) { if (xb_ld(&(bar)[XB_TMO])) break; if (_sp > XB_SPIN_CAP) { atomicAdd(&(bar)[XB_TMO], 1u); break; } } } } while (0)
; __device__ __forceinline__ void xcd_barrier(const XcdBarrier& b) {
;     ...
;             else XB_SPIN(xb_ld(&bar[XB_TOPGEN]) == tg, bar);
.LBB0_461:
	global_load_dword v2, v195, s[8:9] sc1
	s_add_i32 s16, s16, 1
	s_mov_b64 s[30:31], -1
	s_waitcnt vmcnt(0)
	v_cmp_ge_u32_e32 vcc, v2, v4
	s_orn2_b64 s[24:25], vcc, exec
	s_branch .LBB0_456

; __device__ __forceinline__ unsigned xb_ld(unsigned* p)              { return __hip_atomic_load(p, __ATOMIC_RELAXED, __HIP_MEMORY_SCOPE_AGENT); }
; __device__ __forceinline__ unsigned xb_add(unsigned* p, unsigned v) { return __hip_atomic_fetch_add(p, v, __ATOMIC_RELAXED, __HIP_MEMORY_SCOPE_AGENT); }
; #define XB_SPIN(cond, bar) do { unsigned _sp = 0; while (cond) { __builtin_amdgcn_s_sleep(1); \
;     if ((++_sp & 255u) == 0u) { if (xb_ld(&(bar)[XB_TMO])) break; if (_sp > XB_SPIN_CAP) { atomicAdd(&(bar)[XB_TMO], 1u); break; } } } } while (0)
; __device__ __forceinline__ void xcd_barrier(const XcdBarrier& b) {
;     ...
;             if (og + 1u == (tg + 1u) * nx) xb_add(&bar[XB_TOPGEN], 1u);
;             else XB_SPIN(xb_ld(&bar[XB_TOPGEN]) == tg, bar);
;             __builtin_amdgcn_fence(__ATOMIC_ACQUIRE, "agent");
;             xb_add(&bar[XB_XGEN(b.x)], 1u);
.LBB0_465:
	s_or_b64 exec, exec, s[10:11]
	s_and_saveexec_b64 s[8:9], s[14:15]
	s_cbranch_execz .LBB0_467
.LBB0_467:
	s_or_b64 exec, exec, s[8:9]
	s_mov_b64 s[8:9], exec
	v_mbcnt_lo_u32_b32 v2, s8, 0
	v_mbcnt_hi_u32_b32 v2, s9, v2
	v_cmp_eq_u32_e32 vcc, 0, v2
	s_waitcnt vmcnt(0)
	buffer_inv sc1
	s_and_saveexec_b64 s[10:11], vcc
	s_cbranch_execz .LBB0_469
	s_bcnt1_i32_b64 s8, s[8:9]
	v_mov_b32_e32 v2, s8
	v_mov_b32_e32 v3, 0x2000

; __device__ __forceinline__ unsigned xb_ld(unsigned* p)              { return __hip_atomic_load(p, __ATOMIC_RELAXED, __HIP_MEMORY_SCOPE_AGENT); }
; __device__ __forceinline__ unsigned xb_add(unsigned* p, unsigned v) { return __hip_atomic_fetch_add(p, v, __ATOMIC_RELAXED, __HIP_MEMORY_SCOPE_AGENT); }
; #define XB_SPIN(cond, bar) do { unsigned _sp = 0; while (cond) { __builtin_amdgcn_s_sleep(1); \
;     if ((++_sp & 255u) == 0u) { if (xb_ld(&(bar)[XB_TMO])) break; if (_sp > XB_SPIN_CAP) { atomicAdd(&(bar)[XB_TMO], 1u); break; } } } } while (0)
; __device__ __forceinline__ void xcd_barrier(const XcdBarrier& b) {
;     ...
;             const unsigned og = xb_add(&bar[XB_TOP], 1u);
;             const unsigned tg = og / nx;
;             if (og + 1u == (tg + 1u) * nx) xb_add(&bar[XB_TOPGEN], 1u);
;             else XB_SPIN(xb_ld(&bar[XB_TOPGEN]) == tg, bar);
.LBB0_540:
	s_or_b64 exec, exec, s[24:25]
	v_cvt_f32_u32_e32 v6, v4
	s_waitcnt vmcnt(0)
	v_readfirstlane_b32 s14, v5
	v_sub_u32_e32 v5, 0, v4
	v_rcp_iflag_f32_e32 v6, v6
	v_add_u32_e32 v7, s14, v3
	v_mul_f32_e32 v6, 0x4f7ffffe, v6
	v_cvt_u32_f32_e32 v6, v6
	v_mul_lo_u32 v3, v5, v6
	v_mul_hi_u32 v3, v6, v3
	v_add_u32_e32 v3, v6, v3
	v_mul_hi_u32 v3, v7, v3
	v_mul_lo_u32 v5, v3, v4
	v_sub_u32_e32 v5, v7, v5
	v_add_u32_e32 v6, 1, v3
	v_cmp_ge_u32_e32 vcc, v5, v4
	s_nop 1
	v_cndmask_b32_e32 v3, v3, v6, vcc
	v_sub_u32_e32 v6, v5, v4
	v_cndmask_b32_e32 v5, v5, v6, vcc
	v_add_u32_e32 v6, 1, v3
	v_cmp_ge_u32_e32 vcc, v5, v4
	v_add_u32_e32 v5, 1, v7
	s_nop 0
	v_cndmask_b32_e32 v3, v3, v6, vcc
	v_mul_lo_u32 v6, v4, v3
	v_add_u32_e32 v4, v6, v4
	v_cmp_ne_u32_e32 vcc, v5, v4
	s_and_saveexec_b64 s[14:15], vcc
	s_xor_b64 s[14:15], exec, s[14:15]
	s_cbranch_execz .LBB0_554
	s_waitcnt lgkmcnt(0)
	v_mad_u32_u24 v3, v2, v3, v2
	s_add_u32 s36, s34, 0x7400
	s_addc_u32 s37, s35, 0
	v_mov_b32_e32 v2, 0
	global_load_dword v2, v2, s[36:37] sc1
	s_waitcnt vmcnt(0)
	v_cmp_gt_u32_e32 vcc, v3, v2
	s_and_saveexec_b64 s[28:29], vcc
	s_cbranch_execz .LBB0_553
	s_add_u32 s30, s34, 0x4200
	s_addc_u32 s31, s35, 0
	s_mov_b32 s16, 1
	s_mov_b64 s[40:41], 0
	s_branch .LBB0_544

; __device__ __forceinline__ unsigned xb_ld(unsigned* p)              { return __hip_atomic_load(p, __ATOMIC_RELAXED, __HIP_MEMORY_SCOPE_AGENT); }
; #define XB_SPIN(cond, bar) do { unsigned _sp = 0; while (cond) { __builtin_amdgcn_s_sleep(1); \
;     if ((++_sp & 255u) == 0u) { if (xb_ld(&(bar)[XB_TMO])) break; if (_sp > XB_SPIN_CAP) { atomicAdd(&(bar)[XB_TMO], 1u); break; } } } } while (0)
; __device__ __forceinline__ void xcd_barrier(const XcdBarrier& b) {
;     ...
;             else XB_SPIN(xb_ld(&bar[XB_TOPGEN]) == tg, bar);
.LBB0_548:
	global_load_dword v2, v195, s[36:37] sc1
	s_add_i32 s16, s16, 1
	s_mov_b64 s[42:43], -1
	s_waitcnt vmcnt(0)
	v_cmp_ge_u32_e32 vcc, v2, v3
	s_orn2_b64 s[24:25], vcc, exec
	s_branch .LBB0_543

; __device__ __forceinline__ unsigned xb_ld(unsigned* p)              { return __hip_atomic_load(p, __ATOMIC_RELAXED, __HIP_MEMORY_SCOPE_AGENT); }
; __device__ __forceinline__ unsigned xb_add(unsigned* p, unsigned v) { return __hip_atomic_fetch_add(p, v, __ATOMIC_RELAXED, __HIP_MEMORY_SCOPE_AGENT); }
; #define XB_SPIN(cond, bar) do { unsigned _sp = 0; while (cond) { __builtin_amdgcn_s_sleep(1); \
;     if ((++_sp & 255u) == 0u) { if (xb_ld(&(bar)[XB_TMO])) break; if (_sp > XB_SPIN_CAP) { atomicAdd(&(bar)[XB_TMO], 1u); break; } } } } while (0)
; __device__ __forceinline__ void xcd_barrier(const XcdBarrier& b) {
;     ...
;             const unsigned og = xb_add(&bar[XB_TOP], 1u);
;             const unsigned tg = og / nx;
;             if (og + 1u == (tg + 1u) * nx) xb_add(&bar[XB_TOPGEN], 1u);
;             else XB_SPIN(xb_ld(&bar[XB_TOPGEN]) == tg, bar);
.LBB0_557:
	s_or_b64 exec, exec, s[24:25]
	s_waitcnt vmcnt(0)
	v_readfirstlane_b32 s14, v4
	v_cvt_f32_u32_e32 v4, v2
	v_sub_u32_e32 v5, 0, v2
	v_add_u32_e32 v3, s14, v3
	s_add_u32 s14, s34, 0x7400
	v_rcp_iflag_f32_e32 v4, v4
	s_addc_u32 s15, s35, 0
	s_mov_b64 s[24:25], -1
	v_mul_f32_e32 v4, 0x4f7ffffe, v4
	v_cvt_u32_f32_e32 v4, v4
	v_mul_lo_u32 v5, v5, v4
	v_mul_hi_u32 v5, v4, v5
	v_add_u32_e32 v4, v4, v5
	v_mul_hi_u32 v4, v3, v4
	v_mul_lo_u32 v5, v4, v2
	v_sub_u32_e32 v5, v3, v5
	v_cmp_ge_u32_e32 vcc, v5, v2
	v_add_u32_e32 v6, 1, v4
	v_add_u32_e32 v3, 1, v3
	v_cndmask_b32_e32 v4, v4, v6, vcc
	v_sub_u32_e32 v6, v5, v2
	v_cndmask_b32_e32 v5, v5, v6, vcc
	v_cmp_ge_u32_e32 vcc, v5, v2
	v_add_u32_e32 v5, 1, v4
	s_nop 0
	v_cndmask_b32_e32 v4, v4, v5, vcc
	v_mul_lo_u32 v5, v2, v4
	v_add_u32_e32 v2, v5, v2
	v_cmp_ne_u32_e32 vcc, v3, v2
	v_mov_b32_e32 v4, v2
	v_mov_b64_e32 v[2:3], s[14:15]
	s_and_saveexec_b64 s[28:29], vcc
	s_cbranch_execz .LBB0_569
	global_load_dword v2, v195, s[14:15] sc1
	s_mov_b64 s[24:25], 0
	s_waitcnt vmcnt(0)
	v_cmp_gt_u32_e32 vcc, v4, v2
	s_and_saveexec_b64 s[36:37], vcc
	s_cbranch_execz .LBB0_568
	s_add_u32 s30, s34, 0x4200
	s_addc_u32 s31, s35, 0
	s_mov_b32 s16, 1
	s_mov_b64 s[40:41], 0
	s_branch .LBB0_561

; __device__ __forceinline__ unsigned xb_ld(unsigned* p)              { return __hip_atomic_load(p, __ATOMIC_RELAXED, __HIP_MEMORY_SCOPE_AGENT); }
; #define XB_SPIN(cond, bar) do { unsigned _sp = 0; while (cond) { __builtin_amdgcn_s_sleep(1); \
;     if ((++_sp & 255u) == 0u) { if (xb_ld(&(bar)[XB_TMO])) break; if (_sp > XB_SPIN_CAP) { atomicAdd(&(bar)[XB_TMO], 1u); break; } } } } while (0)
; __device__ __forceinline__ void xcd_barrier(const XcdBarrier& b) {
;     ...
;             else XB_SPIN(xb_ld(&bar[XB_TOPGEN]) == tg, bar);
.LBB0_565:
	global_load_dword v2, v195, s[14:15] sc1
	s_add_i32 s16, s16, 1
	s_mov_b64 s[42:43], -1
	s_waitcnt vmcnt(0)
	v_cmp_ge_u32_e32 vcc, v2, v4
	s_orn2_b64 s[24:25], vcc, exec
	s_branch .LBB0_560

; __device__ __forceinline__ unsigned xb_ld(unsigned* p)              { return __hip_atomic_load(p, __ATOMIC_RELAXED, __HIP_MEMORY_SCOPE_AGENT); }
; __device__ __forceinline__ unsigned xb_add(unsigned* p, unsigned v) { return __hip_atomic_fetch_add(p, v, __ATOMIC_RELAXED, __HIP_MEMORY_SCOPE_AGENT); }
; #define XB_SPIN(cond, bar) do { unsigned _sp = 0; while (cond) { __builtin_amdgcn_s_sleep(1); \
;     if ((++_sp & 255u) == 0u) { if (xb_ld(&(bar)[XB_TMO])) break; if (_sp > XB_SPIN_CAP) { atomicAdd(&(bar)[XB_TMO], 1u); break; } } } } while (0)
; __device__ __forceinline__ void xcd_barrier(const XcdBarrier& b) {
;     ...
;             if (og + 1u == (tg + 1u) * nx) xb_add(&bar[XB_TOPGEN], 1u);
;             else XB_SPIN(xb_ld(&bar[XB_TOPGEN]) == tg, bar);
;             __builtin_amdgcn_fence(__ATOMIC_ACQUIRE, "agent");
;             xb_add(&bar[XB_XGEN(b.x)], 1u);
.LBB0_569:
	s_or_b64 exec, exec, s[28:29]
	s_and_saveexec_b64 s[14:15], s[24:25]
	s_cbranch_execz .LBB0_571
.LBB0_571:
	s_or_b64 exec, exec, s[14:15]
	s_mov_b64 s[14:15], exec
	v_mbcnt_lo_u32_b32 v2, s14, 0
	v_mbcnt_hi_u32_b32 v2, s15, v2
	v_cmp_eq_u32_e32 vcc, 0, v2
	s_waitcnt vmcnt(0)
	buffer_inv sc1
	s_and_saveexec_b64 s[24:25], vcc
	s_cbranch_execz .LBB0_573
	s_bcnt1_i32_b64 s14, s[14:15]
	v_mov_b32_e32 v2, s14
	v_mov_b32_e32 v3, 0x2000

; __device__ __forceinline__ unsigned xb_ld(unsigned* p)              { return __hip_atomic_load(p, __ATOMIC_RELAXED, __HIP_MEMORY_SCOPE_AGENT); }
; __device__ __forceinline__ unsigned xb_add(unsigned* p, unsigned v) { return __hip_atomic_fetch_add(p, v, __ATOMIC_RELAXED, __HIP_MEMORY_SCOPE_AGENT); }
; #define XB_SPIN(cond, bar) do { unsigned _sp = 0; while (cond) { __builtin_amdgcn_s_sleep(1); \
;     if ((++_sp & 255u) == 0u) { if (xb_ld(&(bar)[XB_TMO])) break; if (_sp > XB_SPIN_CAP) { atomicAdd(&(bar)[XB_TMO], 1u); break; } } } } while (0)
; __device__ __forceinline__ void xcd_barrier(const XcdBarrier& b) {
;     ...
;             if (og + 1u == (tg + 1u) * nx) xb_add(&bar[XB_TOPGEN], 1u);
;             else XB_SPIN(xb_ld(&bar[XB_TOPGEN]) == tg, bar);
;             __builtin_amdgcn_fence(__ATOMIC_ACQUIRE, "agent");
;             xb_add(&bar[XB_XGEN(b.x)], 1u);
.LBB0_632:
	s_or_b64 exec, exec, s[28:29]
	s_and_saveexec_b64 s[14:15], s[24:25]
	s_cbranch_execz .LBB0_634
.LBB0_634:
	s_or_b64 exec, exec, s[14:15]
	s_mov_b64 s[14:15], exec
	v_mbcnt_lo_u32_b32 v2, s14, 0
	v_mbcnt_hi_u32_b32 v2, s15, v2
	v_cmp_eq_u32_e32 vcc, 0, v2
	s_waitcnt vmcnt(0)
	buffer_inv sc1
	s_and_saveexec_b64 s[24:25], vcc
	s_cbranch_execz .LBB0_636
	s_bcnt1_i32_b64 s14, s[14:15]
	v_mov_b32_e32 v2, s14
	v_mov_b32_e32 v3, 0x2000

; __device__ __forceinline__ unsigned xb_ld(unsigned* p)              { return __hip_atomic_load(p, __ATOMIC_RELAXED, __HIP_MEMORY_SCOPE_AGENT); }
; __device__ __forceinline__ unsigned xb_add(unsigned* p, unsigned v) { return __hip_atomic_fetch_add(p, v, __ATOMIC_RELAXED, __HIP_MEMORY_SCOPE_AGENT); }
; #define XB_SPIN(cond, bar) do { unsigned _sp = 0; while (cond) { __builtin_amdgcn_s_sleep(1); \
;     if ((++_sp & 255u) == 0u) { if (xb_ld(&(bar)[XB_TMO])) break; if (_sp > XB_SPIN_CAP) { atomicAdd(&(bar)[XB_TMO], 1u); break; } } } } while (0)
; __device__ __forceinline__ void xcd_barrier(const XcdBarrier& b) {
;     ...
;             const unsigned og = xb_add(&bar[XB_TOP], 1u);
;             const unsigned tg = og / nx;
;             if (og + 1u == (tg + 1u) * nx) xb_add(&bar[XB_TOPGEN], 1u);
;             else XB_SPIN(xb_ld(&bar[XB_TOPGEN]) == tg, bar);
.LBB0_689:
	s_or_b64 exec, exec, s[10:11]
	v_cvt_f32_u32_e32 v6, v4
	s_waitcnt vmcnt(0)
	v_readfirstlane_b32 s8, v5
	v_sub_u32_e32 v5, 0, v4
	v_rcp_iflag_f32_e32 v6, v6
	v_add_u32_e32 v7, s8, v3
	v_mul_f32_e32 v6, 0x4f7ffffe, v6
	v_cvt_u32_f32_e32 v6, v6
	v_mul_lo_u32 v3, v5, v6
	v_mul_hi_u32 v3, v6, v3
	v_add_u32_e32 v3, v6, v3
	v_mul_hi_u32 v3, v7, v3
	v_mul_lo_u32 v5, v3, v4
	v_sub_u32_e32 v5, v7, v5
	v_add_u32_e32 v6, 1, v3
	v_cmp_ge_u32_e32 vcc, v5, v4
	s_nop 1
	v_cndmask_b32_e32 v3, v3, v6, vcc
	v_sub_u32_e32 v6, v5, v4
	v_cndmask_b32_e32 v5, v5, v6, vcc
	v_add_u32_e32 v6, 1, v3
	v_cmp_ge_u32_e32 vcc, v5, v4
	v_add_u32_e32 v5, 1, v7
	s_nop 0
	v_cndmask_b32_e32 v3, v3, v6, vcc
	v_mul_lo_u32 v6, v4, v3
	v_add_u32_e32 v4, v6, v4
	v_cmp_ne_u32_e32 vcc, v5, v4
	s_and_saveexec_b64 s[8:9], vcc
	s_xor_b64 s[8:9], exec, s[8:9]
	s_cbranch_execz .LBB0_703
	s_waitcnt lgkmcnt(0)
	v_mad_u32_u24 v3, v2, v3, v2
	s_add_u32 s20, s34, 0x7400
	s_addc_u32 s21, s35, 0
	v_mov_b32_e32 v2, 0
	global_load_dword v2, v2, s[20:21] sc1
	s_waitcnt vmcnt(0)
	v_cmp_gt_u32_e32 vcc, v3, v2
	s_and_saveexec_b64 s[10:11], vcc
	s_cbranch_execz .LBB0_702
	s_add_u32 s14, s34, 0x4200
	s_addc_u32 s15, s35, 0
	s_mov_b32 s16, 1
	s_mov_b64 s[22:23], 0
	s_branch .LBB0_693

; __device__ __forceinline__ unsigned xb_ld(unsigned* p)              { return __hip_atomic_load(p, __ATOMIC_RELAXED, __HIP_MEMORY_SCOPE_AGENT); }
; #define XB_SPIN(cond, bar) do { unsigned _sp = 0; while (cond) { __builtin_amdgcn_s_sleep(1); \
;     if ((++_sp & 255u) == 0u) { if (xb_ld(&(bar)[XB_TMO])) break; if (_sp > XB_SPIN_CAP) { atomicAdd(&(bar)[XB_TMO], 1u); break; } } } } while (0)
; __device__ __forceinline__ void xcd_barrier(const XcdBarrier& b) {
;     ...
;             else XB_SPIN(xb_ld(&bar[XB_TOPGEN]) == tg, bar);
.LBB0_697:
	global_load_dword v2, v195, s[20:21] sc1
	s_add_i32 s16, s16, 1
	s_mov_b64 s[28:29], -1
	s_waitcnt vmcnt(0)
	v_cmp_ge_u32_e32 vcc, v2, v3
	s_orn2_b64 s[24:25], vcc, exec
	s_branch .LBB0_692

; __device__ __forceinline__ unsigned xb_ld(unsigned* p)              { return __hip_atomic_load(p, __ATOMIC_RELAXED, __HIP_MEMORY_SCOPE_AGENT); }
; __device__ __forceinline__ unsigned xb_add(unsigned* p, unsigned v) { return __hip_atomic_fetch_add(p, v, __ATOMIC_RELAXED, __HIP_MEMORY_SCOPE_AGENT); }
; #define XB_SPIN(cond, bar) do { unsigned _sp = 0; while (cond) { __builtin_amdgcn_s_sleep(1); \
;     if ((++_sp & 255u) == 0u) { if (xb_ld(&(bar)[XB_TMO])) break; if (_sp > XB_SPIN_CAP) { atomicAdd(&(bar)[XB_TMO], 1u); break; } } } } while (0)
; __device__ __forceinline__ void xcd_barrier(const XcdBarrier& b) {
;     ...
;             const unsigned og = xb_add(&bar[XB_TOP], 1u);
;             const unsigned tg = og / nx;
;             if (og + 1u == (tg + 1u) * nx) xb_add(&bar[XB_TOPGEN], 1u);
;             else XB_SPIN(xb_ld(&bar[XB_TOPGEN]) == tg, bar);
.LBB0_706:
	s_or_b64 exec, exec, s[10:11]
	s_waitcnt vmcnt(0)
	v_readfirstlane_b32 s8, v4
	v_cvt_f32_u32_e32 v4, v2
	v_sub_u32_e32 v5, 0, v2
	v_add_u32_e32 v3, s8, v3
	s_add_u32 s8, s34, 0x7400
	v_rcp_iflag_f32_e32 v4, v4
	s_addc_u32 s9, s35, 0
	s_mov_b64 s[14:15], -1
	v_mul_f32_e32 v4, 0x4f7ffffe, v4
	v_cvt_u32_f32_e32 v4, v4
	v_mul_lo_u32 v5, v5, v4
	v_mul_hi_u32 v5, v4, v5
	v_add_u32_e32 v4, v4, v5
	v_mul_hi_u32 v4, v3, v4
	v_mul_lo_u32 v5, v4, v2
	v_sub_u32_e32 v5, v3, v5
	v_cmp_ge_u32_e32 vcc, v5, v2
	v_add_u32_e32 v6, 1, v4
	v_add_u32_e32 v3, 1, v3
	v_cndmask_b32_e32 v4, v4, v6, vcc
	v_sub_u32_e32 v6, v5, v2
	v_cndmask_b32_e32 v5, v5, v6, vcc
	v_cmp_ge_u32_e32 vcc, v5, v2
	v_add_u32_e32 v5, 1, v4
	s_nop 0
	v_cndmask_b32_e32 v4, v4, v5, vcc
	v_mul_lo_u32 v5, v2, v4
	v_add_u32_e32 v2, v5, v2
	v_cmp_ne_u32_e32 vcc, v3, v2
	v_mov_b32_e32 v4, v2
	v_mov_b64_e32 v[2:3], s[8:9]
	s_and_saveexec_b64 s[10:11], vcc
	s_cbranch_execz .LBB0_718
	global_load_dword v2, v195, s[8:9] sc1
	s_mov_b64 s[22:23], 0
	s_waitcnt vmcnt(0)
	v_cmp_gt_u32_e32 vcc, v4, v2
	s_and_saveexec_b64 s[20:21], vcc
	s_cbranch_execz .LBB0_717
	s_add_u32 s14, s34, 0x4200
	s_addc_u32 s15, s35, 0
	s_mov_b32 s16, 1
	s_branch .LBB0_710

; __device__ __forceinline__ unsigned xb_ld(unsigned* p)              { return __hip_atomic_load(p, __ATOMIC_RELAXED, __HIP_MEMORY_SCOPE_AGENT); }
; #define XB_SPIN(cond, bar) do { unsigned _sp = 0; while (cond) { __builtin_amdgcn_s_sleep(1); \
;     if ((++_sp & 255u) == 0u) { if (xb_ld(&(bar)[XB_TMO])) break; if (_sp > XB_SPIN_CAP) { atomicAdd(&(bar)[XB_TMO], 1u); break; } } } } while (0)
; __device__ __forceinline__ void xcd_barrier(const XcdBarrier& b) {
;     ...
;             else XB_SPIN(xb_ld(&bar[XB_TOPGEN]) == tg, bar);
.LBB0_714:
	global_load_dword v2, v195, s[8:9] sc1
	s_add_i32 s16, s16, 1
	s_mov_b64 s[28:29], -1
	s_waitcnt vmcnt(0)
	v_cmp_ge_u32_e32 vcc, v2, v4
	s_orn2_b64 s[24:25], vcc, exec
	s_branch .LBB0_709

; __device__ __forceinline__ unsigned xb_ld(unsigned* p)              { return __hip_atomic_load(p, __ATOMIC_RELAXED, __HIP_MEMORY_SCOPE_AGENT); }
; __device__ __forceinline__ unsigned xb_add(unsigned* p, unsigned v) { return __hip_atomic_fetch_add(p, v, __ATOMIC_RELAXED, __HIP_MEMORY_SCOPE_AGENT); }
; #define XB_SPIN(cond, bar) do { unsigned _sp = 0; while (cond) { __builtin_amdgcn_s_sleep(1); \
;     if ((++_sp & 255u) == 0u) { if (xb_ld(&(bar)[XB_TMO])) break; if (_sp > XB_SPIN_CAP) { atomicAdd(&(bar)[XB_TMO], 1u); break; } } } } while (0)
; __device__ __forceinline__ void xcd_barrier(const XcdBarrier& b) {
;     ...
;             if (og + 1u == (tg + 1u) * nx) xb_add(&bar[XB_TOPGEN], 1u);
;             else XB_SPIN(xb_ld(&bar[XB_TOPGEN]) == tg, bar);
;             __builtin_amdgcn_fence(__ATOMIC_ACQUIRE, "agent");
;             xb_add(&bar[XB_XGEN(b.x)], 1u);
.LBB0_718:
	s_or_b64 exec, exec, s[10:11]
	s_and_saveexec_b64 s[8:9], s[14:15]
	s_cbranch_execz .LBB0_720
.LBB0_720:
	s_or_b64 exec, exec, s[8:9]
	s_mov_b64 s[8:9], exec
	v_mbcnt_lo_u32_b32 v2, s8, 0
	v_mbcnt_hi_u32_b32 v2, s9, v2
	v_cmp_eq_u32_e32 vcc, 0, v2
	s_waitcnt vmcnt(0)
	buffer_inv sc1
	s_and_saveexec_b64 s[10:11], vcc
	s_cbranch_execz .LBB0_722
	s_bcnt1_i32_b64 s8, s[8:9]
	v_mov_b32_e32 v2, s8
	v_mov_b32_e32 v3, 0x2000

; __device__ __forceinline__ unsigned xb_ld(unsigned* p)              { return __hip_atomic_load(p, __ATOMIC_RELAXED, __HIP_MEMORY_SCOPE_AGENT); }
; __device__ __forceinline__ unsigned xb_add(unsigned* p, unsigned v) { return __hip_atomic_fetch_add(p, v, __ATOMIC_RELAXED, __HIP_MEMORY_SCOPE_AGENT); }
; #define XB_SPIN(cond, bar) do { unsigned _sp = 0; while (cond) { __builtin_amdgcn_s_sleep(1); \
;     if ((++_sp & 255u) == 0u) { if (xb_ld(&(bar)[XB_TMO])) break; if (_sp > XB_SPIN_CAP) { atomicAdd(&(bar)[XB_TMO], 1u); break; } } } } while (0)
; __device__ __forceinline__ void xcd_barrier(const XcdBarrier& b) {
;     ...
;             const unsigned og = xb_add(&bar[XB_TOP], 1u);
;             const unsigned tg = og / nx;
;             if (og + 1u == (tg + 1u) * nx) xb_add(&bar[XB_TOPGEN], 1u);
;             else XB_SPIN(xb_ld(&bar[XB_TOPGEN]) == tg, bar);
.LBB0_774:
	s_or_b64 exec, exec, s[14:15]
	v_cvt_f32_u32_e32 v5, v3
	s_waitcnt vmcnt(0)
	v_readfirstlane_b32 s3, v4
	v_sub_u32_e32 v4, 0, v3
	v_rcp_iflag_f32_e32 v5, v5
	v_add_u32_e32 v6, s3, v1
	v_mul_f32_e32 v5, 0x4f7ffffe, v5
	v_cvt_u32_f32_e32 v5, v5
	v_mul_lo_u32 v1, v4, v5
	v_mul_hi_u32 v1, v5, v1
	v_add_u32_e32 v1, v5, v1
	v_mul_hi_u32 v1, v6, v1
	v_mul_lo_u32 v4, v1, v3
	v_sub_u32_e32 v4, v6, v4
	v_add_u32_e32 v5, 1, v1
	v_cmp_ge_u32_e32 vcc, v4, v3
	s_nop 1
	v_cndmask_b32_e32 v1, v1, v5, vcc
	v_sub_u32_e32 v5, v4, v3
	v_cndmask_b32_e32 v4, v4, v5, vcc
	v_add_u32_e32 v5, 1, v1
	v_cmp_ge_u32_e32 vcc, v4, v3
	v_add_u32_e32 v4, 1, v6
	s_nop 0
	v_cndmask_b32_e32 v1, v1, v5, vcc
	v_mul_lo_u32 v5, v3, v1
	v_add_u32_e32 v3, v5, v3
	v_cmp_ne_u32_e32 vcc, v4, v3
	s_and_saveexec_b64 s[8:9], vcc
	s_xor_b64 s[8:9], exec, s[8:9]
	s_cbranch_execz .LBB0_788
	s_waitcnt lgkmcnt(0)
	v_mad_u32_u24 v1, v2, v1, v2
	s_add_u32 s22, s34, 0x7400
	s_addc_u32 s23, s35, 0
	v_mov_b32_e32 v2, 0
	global_load_dword v2, v2, s[22:23] sc1
	s_waitcnt vmcnt(0)
	v_cmp_gt_u32_e32 vcc, v1, v2
	s_and_saveexec_b64 s[14:15], vcc
	s_cbranch_execz .LBB0_787
	s_add_u32 s20, s34, 0x4200
	s_addc_u32 s21, s35, 0
	s_mov_b32 s3, 1
	s_mov_b64 s[26:27], 0
	s_branch .LBB0_778

; __device__ __forceinline__ unsigned xb_ld(unsigned* p)              { return __hip_atomic_load(p, __ATOMIC_RELAXED, __HIP_MEMORY_SCOPE_AGENT); }
; #define XB_SPIN(cond, bar) do { unsigned _sp = 0; while (cond) { __builtin_amdgcn_s_sleep(1); \
;     if ((++_sp & 255u) == 0u) { if (xb_ld(&(bar)[XB_TMO])) break; if (_sp > XB_SPIN_CAP) { atomicAdd(&(bar)[XB_TMO], 1u); break; } } } } while (0)
; __device__ __forceinline__ void xcd_barrier(const XcdBarrier& b) {
;     ...
;             else XB_SPIN(xb_ld(&bar[XB_TOPGEN]) == tg, bar);
.LBB0_782:
	global_load_dword v2, v195, s[22:23] sc1
	s_add_i32 s3, s3, 1
	s_mov_b64 s[30:31], -1
	s_waitcnt vmcnt(0)
	v_cmp_ge_u32_e32 vcc, v2, v1
	s_orn2_b64 s[24:25], vcc, exec
	s_branch .LBB0_777

; __device__ __forceinline__ unsigned xb_ld(unsigned* p)              { return __hip_atomic_load(p, __ATOMIC_RELAXED, __HIP_MEMORY_SCOPE_AGENT); }
; __device__ __forceinline__ unsigned xb_add(unsigned* p, unsigned v) { return __hip_atomic_fetch_add(p, v, __ATOMIC_RELAXED, __HIP_MEMORY_SCOPE_AGENT); }
; #define XB_SPIN(cond, bar) do { unsigned _sp = 0; while (cond) { __builtin_amdgcn_s_sleep(1); \
;     if ((++_sp & 255u) == 0u) { if (xb_ld(&(bar)[XB_TMO])) break; if (_sp > XB_SPIN_CAP) { atomicAdd(&(bar)[XB_TMO], 1u); break; } } } } while (0)
; __device__ __forceinline__ void xcd_barrier(const XcdBarrier& b) {
;     ...
;             const unsigned og = xb_add(&bar[XB_TOP], 1u);
;             const unsigned tg = og / nx;
;             if (og + 1u == (tg + 1u) * nx) xb_add(&bar[XB_TOPGEN], 1u);
;             else XB_SPIN(xb_ld(&bar[XB_TOPGEN]) == tg, bar);
.LBB0_791:
	s_or_b64 exec, exec, s[14:15]
	s_waitcnt vmcnt(0)
	v_readfirstlane_b32 s3, v3
	v_sub_u32_e32 v4, 0, v2
	s_add_u32 s8, s34, 0x7400
	v_add_u32_e32 v3, s3, v1
	v_cvt_f32_u32_e32 v1, v2
	s_addc_u32 s9, s35, 0
	s_mov_b64 s[20:21], -1
	v_rcp_iflag_f32_e32 v1, v1
	s_nop 0
	v_mul_f32_e32 v1, 0x4f7ffffe, v1
	v_cvt_u32_f32_e32 v1, v1
	v_mul_lo_u32 v4, v4, v1
	v_mul_hi_u32 v4, v1, v4
	v_add_u32_e32 v1, v1, v4
	v_mul_hi_u32 v1, v3, v1
	v_mul_lo_u32 v4, v1, v2
	v_sub_u32_e32 v4, v3, v4
	v_cmp_ge_u32_e32 vcc, v4, v2
	v_add_u32_e32 v5, 1, v1
	v_add_u32_e32 v3, 1, v3
	v_cndmask_b32_e32 v1, v1, v5, vcc
	v_sub_u32_e32 v5, v4, v2
	v_cndmask_b32_e32 v4, v4, v5, vcc
	v_cmp_ge_u32_e32 vcc, v4, v2
	v_add_u32_e32 v4, 1, v1
	s_nop 0
	v_cndmask_b32_e32 v1, v1, v4, vcc
	v_mul_lo_u32 v4, v2, v1
	v_add_u32_e32 v2, v4, v2
	v_cmp_ne_u32_e32 vcc, v3, v2
	v_mov_b32_e32 v1, v2
	v_mov_b64_e32 v[2:3], s[8:9]
	s_and_saveexec_b64 s[14:15], vcc
	s_cbranch_execz .LBB0_803
	global_load_dword v2, v195, s[8:9] sc1
	s_mov_b64 s[24:25], 0
	s_waitcnt vmcnt(0)
	v_cmp_gt_u32_e32 vcc, v1, v2
	s_and_saveexec_b64 s[22:23], vcc
	s_cbranch_execz .LBB0_802
	s_add_u32 s20, s34, 0x4200
	s_addc_u32 s21, s35, 0
	s_mov_b32 s3, 1
	s_mov_b64 s[26:27], 0
	s_branch .LBB0_795

; __device__ __forceinline__ unsigned xb_ld(unsigned* p)              { return __hip_atomic_load(p, __ATOMIC_RELAXED, __HIP_MEMORY_SCOPE_AGENT); }
; #define XB_SPIN(cond, bar) do { unsigned _sp = 0; while (cond) { __builtin_amdgcn_s_sleep(1); \
;     if ((++_sp & 255u) == 0u) { if (xb_ld(&(bar)[XB_TMO])) break; if (_sp > XB_SPIN_CAP) { atomicAdd(&(bar)[XB_TMO], 1u); break; } } } } while (0)
; __device__ __forceinline__ void xcd_barrier(const XcdBarrier& b) {
;     ...
;             else XB_SPIN(xb_ld(&bar[XB_TOPGEN]) == tg, bar);
.LBB0_799:
	global_load_dword v2, v195, s[8:9] sc1
	s_add_i32 s3, s3, 1
	s_mov_b64 s[30:31], -1
	s_waitcnt vmcnt(0)
	v_cmp_ge_u32_e32 vcc, v2, v1
	s_orn2_b64 s[24:25], vcc, exec
	s_branch .LBB0_794

; __device__ __forceinline__ unsigned xb_ld(unsigned* p)              { return __hip_atomic_load(p, __ATOMIC_RELAXED, __HIP_MEMORY_SCOPE_AGENT); }
; __device__ __forceinline__ unsigned xb_add(unsigned* p, unsigned v) { return __hip_atomic_fetch_add(p, v, __ATOMIC_RELAXED, __HIP_MEMORY_SCOPE_AGENT); }
; #define XB_SPIN(cond, bar) do { unsigned _sp = 0; while (cond) { __builtin_amdgcn_s_sleep(1); \
;     if ((++_sp & 255u) == 0u) { if (xb_ld(&(bar)[XB_TMO])) break; if (_sp > XB_SPIN_CAP) { atomicAdd(&(bar)[XB_TMO], 1u); break; } } } } while (0)
; __device__ __forceinline__ void xcd_barrier(const XcdBarrier& b) {
;     ...
;             if (og + 1u == (tg + 1u) * nx) xb_add(&bar[XB_TOPGEN], 1u);
;             else XB_SPIN(xb_ld(&bar[XB_TOPGEN]) == tg, bar);
;             __builtin_amdgcn_fence(__ATOMIC_ACQUIRE, "agent");
;             xb_add(&bar[XB_XGEN(b.x)], 1u);
.LBB0_803:
	s_or_b64 exec, exec, s[14:15]
	s_and_saveexec_b64 s[8:9], s[20:21]
	s_cbranch_execz .LBB0_805
.LBB0_805:
	s_or_b64 exec, exec, s[8:9]
	s_mov_b64 s[8:9], exec
	v_mbcnt_lo_u32_b32 v1, s8, 0
	v_mbcnt_hi_u32_b32 v1, s9, v1
	v_cmp_eq_u32_e32 vcc, 0, v1
	s_waitcnt vmcnt(0)
	buffer_inv sc1
	s_and_saveexec_b64 s[14:15], vcc
	s_cbranch_execz .LBB0_807
	s_bcnt1_i32_b64 s3, s[8:9]
	v_mov_b32_e32 v1, s3
	v_mov_b32_e32 v2, 0x2000

; __device__ __forceinline__ unsigned xb_ld(unsigned* p)              { return __hip_atomic_load(p, __ATOMIC_RELAXED, __HIP_MEMORY_SCOPE_AGENT); }
; __device__ __forceinline__ unsigned xb_add(unsigned* p, unsigned v) { return __hip_atomic_fetch_add(p, v, __ATOMIC_RELAXED, __HIP_MEMORY_SCOPE_AGENT); }
; #define XB_SPIN(cond, bar) do { unsigned _sp = 0; while (cond) { __builtin_amdgcn_s_sleep(1); \
;     if ((++_sp & 255u) == 0u) { if (xb_ld(&(bar)[XB_TMO])) break; if (_sp > XB_SPIN_CAP) { atomicAdd(&(bar)[XB_TMO], 1u); break; } } } } while (0)
; __device__ __forceinline__ void xcd_barrier(const XcdBarrier& b) {
;     ...
;             const unsigned og = xb_add(&bar[XB_TOP], 1u);
;             const unsigned tg = og / nx;
;             if (og + 1u == (tg + 1u) * nx) xb_add(&bar[XB_TOPGEN], 1u);
;             else XB_SPIN(xb_ld(&bar[XB_TOPGEN]) == tg, bar);
.LBB0_901:
	s_or_b64 exec, exec, s[14:15]
	v_cvt_f32_u32_e32 v5, v3
	s_waitcnt vmcnt(0)
	v_readfirstlane_b32 s3, v4
	v_sub_u32_e32 v4, 0, v3
	v_rcp_iflag_f32_e32 v5, v5
	v_add_u32_e32 v6, s3, v1
	v_mul_f32_e32 v5, 0x4f7ffffe, v5
	v_cvt_u32_f32_e32 v5, v5
	v_mul_lo_u32 v1, v4, v5
	v_mul_hi_u32 v1, v5, v1
	v_add_u32_e32 v1, v5, v1
	v_mul_hi_u32 v1, v6, v1
	v_mul_lo_u32 v4, v1, v3
	v_sub_u32_e32 v4, v6, v4
	v_add_u32_e32 v5, 1, v1
	v_cmp_ge_u32_e32 vcc, v4, v3
	s_nop 1
	v_cndmask_b32_e32 v1, v1, v5, vcc
	v_sub_u32_e32 v5, v4, v3
	v_cndmask_b32_e32 v4, v4, v5, vcc
	v_add_u32_e32 v5, 1, v1
	v_cmp_ge_u32_e32 vcc, v4, v3
	v_add_u32_e32 v4, 1, v6
	s_nop 0
	v_cndmask_b32_e32 v1, v1, v5, vcc
	v_mul_lo_u32 v5, v3, v1
	v_add_u32_e32 v3, v5, v3
	v_cmp_ne_u32_e32 vcc, v4, v3
	s_and_saveexec_b64 s[8:9], vcc
	s_xor_b64 s[8:9], exec, s[8:9]
	s_cbranch_execz .LBB0_915
	s_waitcnt lgkmcnt(0)
	v_mad_u32_u24 v1, v2, v1, v2
	s_add_u32 s26, s34, 0x7400
	s_addc_u32 s27, s35, 0
	v_mov_b32_e32 v2, 0
	global_load_dword v2, v2, s[26:27] sc1
	s_waitcnt vmcnt(0)
	v_cmp_gt_u32_e32 vcc, v1, v2
	s_and_saveexec_b64 s[14:15], vcc
	s_cbranch_execz .LBB0_914
	s_add_u32 s22, s34, 0x4200
	s_addc_u32 s23, s35, 0
	s_mov_b32 s3, 1
	s_mov_b64 s[28:29], 0
	s_branch .LBB0_905

; __device__ __forceinline__ unsigned xb_ld(unsigned* p)              { return __hip_atomic_load(p, __ATOMIC_RELAXED, __HIP_MEMORY_SCOPE_AGENT); }
; __device__ __forceinline__ unsigned xb_add(unsigned* p, unsigned v) { return __hip_atomic_fetch_add(p, v, __ATOMIC_RELAXED, __HIP_MEMORY_SCOPE_AGENT); }
; #define XB_SPIN(cond, bar) do { unsigned _sp = 0; while (cond) { __builtin_amdgcn_s_sleep(1); \
;     if ((++_sp & 255u) == 0u) { if (xb_ld(&(bar)[XB_TMO])) break; if (_sp > XB_SPIN_CAP) { atomicAdd(&(bar)[XB_TMO], 1u); break; } } } } while (0)
; __device__ __forceinline__ void xcd_barrier(const XcdBarrier& b) {
;     ...
;             const unsigned tg = og / nx;
;             if (og + 1u == (tg + 1u) * nx) xb_add(&bar[XB_TOPGEN], 1u);
;             else XB_SPIN(xb_ld(&bar[XB_TOPGEN]) == tg, bar);
.LBB0_909:
	global_load_dword v2, v195, s[26:27] sc1
	s_add_i32 s3, s3, 1
	s_mov_b64 s[36:37], -1
	s_waitcnt vmcnt(0)
	v_cmp_ge_u32_e32 vcc, v2, v1
	s_orn2_b64 s[24:25], vcc, exec
	s_branch .LBB0_904

; __device__ __forceinline__ unsigned xb_ld(unsigned* p)              { return __hip_atomic_load(p, __ATOMIC_RELAXED, __HIP_MEMORY_SCOPE_AGENT); }
; __device__ __forceinline__ unsigned xb_add(unsigned* p, unsigned v) { return __hip_atomic_fetch_add(p, v, __ATOMIC_RELAXED, __HIP_MEMORY_SCOPE_AGENT); }
; #define XB_SPIN(cond, bar) do { unsigned _sp = 0; while (cond) { __builtin_amdgcn_s_sleep(1); \
;     if ((++_sp & 255u) == 0u) { if (xb_ld(&(bar)[XB_TMO])) break; if (_sp > XB_SPIN_CAP) { atomicAdd(&(bar)[XB_TMO], 1u); break; } } } } while (0)
; __device__ __forceinline__ void xcd_barrier(const XcdBarrier& b) {
;     ...
;             const unsigned og = xb_add(&bar[XB_TOP], 1u);
;             const unsigned tg = og / nx;
;             if (og + 1u == (tg + 1u) * nx) xb_add(&bar[XB_TOPGEN], 1u);
;             else XB_SPIN(xb_ld(&bar[XB_TOPGEN]) == tg, bar);
.LBB0_918:
	s_or_b64 exec, exec, s[14:15]
	s_waitcnt vmcnt(0)
	v_readfirstlane_b32 s3, v3
	v_sub_u32_e32 v4, 0, v2
	s_add_u32 s8, s34, 0x7400
	v_add_u32_e32 v3, s3, v1
	v_cvt_f32_u32_e32 v1, v2
	s_addc_u32 s9, s35, 0
	s_mov_b64 s[22:23], -1
	v_rcp_iflag_f32_e32 v1, v1
	s_nop 0
	v_mul_f32_e32 v1, 0x4f7ffffe, v1
	v_cvt_u32_f32_e32 v1, v1
	v_mul_lo_u32 v4, v4, v1
	v_mul_hi_u32 v4, v1, v4
	v_add_u32_e32 v1, v1, v4
	v_mul_hi_u32 v1, v3, v1
	v_mul_lo_u32 v4, v1, v2
	v_sub_u32_e32 v4, v3, v4
	v_cmp_ge_u32_e32 vcc, v4, v2
	v_add_u32_e32 v5, 1, v1
	v_add_u32_e32 v3, 1, v3
	v_cndmask_b32_e32 v1, v1, v5, vcc
	v_sub_u32_e32 v5, v4, v2
	v_cndmask_b32_e32 v4, v4, v5, vcc
	v_cmp_ge_u32_e32 vcc, v4, v2
	v_add_u32_e32 v4, 1, v1
	s_nop 0
	v_cndmask_b32_e32 v1, v1, v4, vcc
	v_mul_lo_u32 v4, v2, v1
	v_add_u32_e32 v2, v4, v2
	v_cmp_ne_u32_e32 vcc, v3, v2
	v_mov_b32_e32 v1, v2
	v_mov_b64_e32 v[2:3], s[8:9]
	s_and_saveexec_b64 s[14:15], vcc
	s_cbranch_execz .LBB0_930
	global_load_dword v2, v195, s[8:9] sc1
	s_mov_b64 s[24:25], 0
	s_waitcnt vmcnt(0)
	v_cmp_gt_u32_e32 vcc, v1, v2
	s_and_saveexec_b64 s[26:27], vcc
	s_cbranch_execz .LBB0_929
	s_add_u32 s22, s34, 0x4200
	s_addc_u32 s23, s35, 0
	s_mov_b32 s3, 1
	s_mov_b64 s[28:29], 0
	s_branch .LBB0_922

; __device__ __forceinline__ unsigned xb_ld(unsigned* p)              { return __hip_atomic_load(p, __ATOMIC_RELAXED, __HIP_MEMORY_SCOPE_AGENT); }
; __device__ __forceinline__ unsigned xb_add(unsigned* p, unsigned v) { return __hip_atomic_fetch_add(p, v, __ATOMIC_RELAXED, __HIP_MEMORY_SCOPE_AGENT); }
; #define XB_SPIN(cond, bar) do { unsigned _sp = 0; while (cond) { __builtin_amdgcn_s_sleep(1); \
;     if ((++_sp & 255u) == 0u) { if (xb_ld(&(bar)[XB_TMO])) break; if (_sp > XB_SPIN_CAP) { atomicAdd(&(bar)[XB_TMO], 1u); break; } } } } while (0)
; __device__ __forceinline__ void xcd_barrier(const XcdBarrier& b) {
;     ...
;             const unsigned tg = og / nx;
;             if (og + 1u == (tg + 1u) * nx) xb_add(&bar[XB_TOPGEN], 1u);
;             else XB_SPIN(xb_ld(&bar[XB_TOPGEN]) == tg, bar);
.LBB0_926:
	global_load_dword v2, v195, s[8:9] sc1
	s_add_i32 s3, s3, 1
	s_mov_b64 s[36:37], -1
	s_waitcnt vmcnt(0)
	v_cmp_ge_u32_e32 vcc, v2, v1
	s_orn2_b64 s[24:25], vcc, exec
	s_branch .LBB0_921

; __device__ __forceinline__ unsigned xb_ld(unsigned* p)              { return __hip_atomic_load(p, __ATOMIC_RELAXED, __HIP_MEMORY_SCOPE_AGENT); }
; __device__ __forceinline__ unsigned xb_add(unsigned* p, unsigned v) { return __hip_atomic_fetch_add(p, v, __ATOMIC_RELAXED, __HIP_MEMORY_SCOPE_AGENT); }
; #define XB_SPIN(cond, bar) do { unsigned _sp = 0; while (cond) { __builtin_amdgcn_s_sleep(1); \
;     if ((++_sp & 255u) == 0u) { if (xb_ld(&(bar)[XB_TMO])) break; if (_sp > XB_SPIN_CAP) { atomicAdd(&(bar)[XB_TMO], 1u); break; } } } } while (0)
; __device__ __forceinline__ void xcd_barrier(const XcdBarrier& b) {
;     ...
;             if (og + 1u == (tg + 1u) * nx) xb_add(&bar[XB_TOPGEN], 1u);
;             else XB_SPIN(xb_ld(&bar[XB_TOPGEN]) == tg, bar);
;             __builtin_amdgcn_fence(__ATOMIC_ACQUIRE, "agent");
;             xb_add(&bar[XB_XGEN(b.x)], 1u);
.LBB0_930:
	s_or_b64 exec, exec, s[14:15]
	s_and_saveexec_b64 s[8:9], s[22:23]
	s_cbranch_execz .LBB0_932
.LBB0_932:
	s_or_b64 exec, exec, s[8:9]
	s_mov_b64 s[8:9], exec
	v_mbcnt_lo_u32_b32 v1, s8, 0
	v_mbcnt_hi_u32_b32 v1, s9, v1
	v_cmp_eq_u32_e32 vcc, 0, v1
	s_waitcnt vmcnt(0)
	buffer_inv sc1
	s_and_saveexec_b64 s[14:15], vcc
	s_cbranch_execz .LBB0_934
	s_bcnt1_i32_b64 s3, s[8:9]
	v_mov_b32_e32 v1, s3
	v_mov_b32_e32 v2, 0x2000

; __device__ __forceinline__ unsigned xb_ld(unsigned* p)              { return __hip_atomic_load(p, __ATOMIC_RELAXED, __HIP_MEMORY_SCOPE_AGENT); }
; __device__ __forceinline__ unsigned xb_add(unsigned* p, unsigned v) { return __hip_atomic_fetch_add(p, v, __ATOMIC_RELAXED, __HIP_MEMORY_SCOPE_AGENT); }
; #define XB_SPIN(cond, bar) do { unsigned _sp = 0; while (cond) { __builtin_amdgcn_s_sleep(1); \
;     if ((++_sp & 255u) == 0u) { if (xb_ld(&(bar)[XB_TMO])) break; if (_sp > XB_SPIN_CAP) { atomicAdd(&(bar)[XB_TMO], 1u); break; } } } } while (0)
; __device__ __forceinline__ void xcd_barrier(const XcdBarrier& b) {
;     ...
;             const unsigned og = xb_add(&bar[XB_TOP], 1u);
;             const unsigned tg = og / nx;
;             if (og + 1u == (tg + 1u) * nx) xb_add(&bar[XB_TOPGEN], 1u);
;             else XB_SPIN(xb_ld(&bar[XB_TOPGEN]) == tg, bar);
.LBB0_1018:
	s_or_b64 exec, exec, s[10:11]
	v_cvt_f32_u32_e32 v5, v3
	s_waitcnt vmcnt(0)
	v_readfirstlane_b32 s3, v4
	v_sub_u32_e32 v4, 0, v3
	v_rcp_iflag_f32_e32 v5, v5
	v_add_u32_e32 v6, s3, v1
	v_mul_f32_e32 v5, 0x4f7ffffe, v5
	v_cvt_u32_f32_e32 v5, v5
	v_mul_lo_u32 v1, v4, v5
	v_mul_hi_u32 v1, v5, v1
	v_add_u32_e32 v1, v5, v1
	v_mul_hi_u32 v1, v6, v1
	v_mul_lo_u32 v4, v1, v3
	v_sub_u32_e32 v4, v6, v4
	v_add_u32_e32 v5, 1, v1
	v_cmp_ge_u32_e32 vcc, v4, v3
	s_nop 1
	v_cndmask_b32_e32 v1, v1, v5, vcc
	v_sub_u32_e32 v5, v4, v3
	v_cndmask_b32_e32 v4, v4, v5, vcc
	v_add_u32_e32 v5, 1, v1
	v_cmp_ge_u32_e32 vcc, v4, v3
	v_add_u32_e32 v4, 1, v6
	s_nop 0
	v_cndmask_b32_e32 v1, v1, v5, vcc
	v_mul_lo_u32 v5, v3, v1
	v_add_u32_e32 v3, v5, v3
	v_cmp_ne_u32_e32 vcc, v4, v3
	s_and_saveexec_b64 s[8:9], vcc
	s_xor_b64 s[8:9], exec, s[8:9]
	s_cbranch_execz .LBB0_1032
	s_waitcnt lgkmcnt(0)
	v_mad_u32_u24 v1, v2, v1, v2
	s_add_u32 s14, s34, 0x7400
	s_addc_u32 s15, s35, 0
	v_mov_b32_e32 v2, 0
	global_load_dword v2, v2, s[14:15] sc1
	s_waitcnt vmcnt(0)
	v_cmp_gt_u32_e32 vcc, v1, v2
	s_and_saveexec_b64 s[10:11], vcc
	s_cbranch_execz .LBB0_1031
	s_add_u32 s12, s34, 0x4200
	s_addc_u32 s13, s35, 0
	s_mov_b32 s3, 1
	s_mov_b64 s[18:19], 0
	s_branch .LBB0_1022

; __device__ __forceinline__ unsigned xb_ld(unsigned* p)              { return __hip_atomic_load(p, __ATOMIC_RELAXED, __HIP_MEMORY_SCOPE_AGENT); }
; __device__ __forceinline__ unsigned xb_add(unsigned* p, unsigned v) { return __hip_atomic_fetch_add(p, v, __ATOMIC_RELAXED, __HIP_MEMORY_SCOPE_AGENT); }
; #define XB_SPIN(cond, bar) do { unsigned _sp = 0; while (cond) { __builtin_amdgcn_s_sleep(1); \
;     if ((++_sp & 255u) == 0u) { if (xb_ld(&(bar)[XB_TMO])) break; if (_sp > XB_SPIN_CAP) { atomicAdd(&(bar)[XB_TMO], 1u); break; } } } } while (0)
; __device__ __forceinline__ void xcd_barrier(const XcdBarrier& b) {
;     ...
;             const unsigned tg = og / nx;
;             if (og + 1u == (tg + 1u) * nx) xb_add(&bar[XB_TOPGEN], 1u);
;             else XB_SPIN(xb_ld(&bar[XB_TOPGEN]) == tg, bar);
.LBB0_1026:
	global_load_dword v2, v195, s[14:15] sc1
	s_add_i32 s3, s3, 1
	s_mov_b64 s[26:27], -1
	s_waitcnt vmcnt(0)
	v_cmp_ge_u32_e32 vcc, v2, v1
	s_orn2_b64 s[24:25], vcc, exec
	s_branch .LBB0_1021

; __device__ __forceinline__ unsigned xb_ld(unsigned* p)              { return __hip_atomic_load(p, __ATOMIC_RELAXED, __HIP_MEMORY_SCOPE_AGENT); }
; __device__ __forceinline__ unsigned xb_add(unsigned* p, unsigned v) { return __hip_atomic_fetch_add(p, v, __ATOMIC_RELAXED, __HIP_MEMORY_SCOPE_AGENT); }
; #define XB_SPIN(cond, bar) do { unsigned _sp = 0; while (cond) { __builtin_amdgcn_s_sleep(1); \
;     if ((++_sp & 255u) == 0u) { if (xb_ld(&(bar)[XB_TMO])) break; if (_sp > XB_SPIN_CAP) { atomicAdd(&(bar)[XB_TMO], 1u); break; } } } } while (0)
; __device__ __forceinline__ void xcd_barrier(const XcdBarrier& b) {
;     ...
;             const unsigned og = xb_add(&bar[XB_TOP], 1u);
;             const unsigned tg = og / nx;
;             if (og + 1u == (tg + 1u) * nx) xb_add(&bar[XB_TOPGEN], 1u);
;             else XB_SPIN(xb_ld(&bar[XB_TOPGEN]) == tg, bar);
.LBB0_1035:
	s_or_b64 exec, exec, s[10:11]
	s_waitcnt vmcnt(0)
	v_readfirstlane_b32 s3, v3
	v_sub_u32_e32 v4, 0, v2
	s_add_u32 s8, s34, 0x7400
	v_add_u32_e32 v3, s3, v1
	v_cvt_f32_u32_e32 v1, v2
	s_addc_u32 s9, s35, 0
	s_mov_b64 s[12:13], -1
	v_rcp_iflag_f32_e32 v1, v1
	s_nop 0
	v_mul_f32_e32 v1, 0x4f7ffffe, v1
	v_cvt_u32_f32_e32 v1, v1
	v_mul_lo_u32 v4, v4, v1
	v_mul_hi_u32 v4, v1, v4
	v_add_u32_e32 v1, v1, v4
	v_mul_hi_u32 v1, v3, v1
	v_mul_lo_u32 v4, v1, v2
	v_sub_u32_e32 v4, v3, v4
	v_cmp_ge_u32_e32 vcc, v4, v2
	v_add_u32_e32 v5, 1, v1
	v_add_u32_e32 v3, 1, v3
	v_cndmask_b32_e32 v1, v1, v5, vcc
	v_sub_u32_e32 v5, v4, v2
	v_cndmask_b32_e32 v4, v4, v5, vcc
	v_cmp_ge_u32_e32 vcc, v4, v2
	v_add_u32_e32 v4, 1, v1
	s_nop 0
	v_cndmask_b32_e32 v1, v1, v4, vcc
	v_mul_lo_u32 v4, v2, v1
	v_add_u32_e32 v2, v4, v2
	v_cmp_ne_u32_e32 vcc, v3, v2
	v_mov_b32_e32 v1, v2
	v_mov_b64_e32 v[2:3], s[8:9]
	s_and_saveexec_b64 s[10:11], vcc
	s_cbranch_execz .LBB0_1047
	global_load_dword v2, v195, s[8:9] sc1
	s_mov_b64 s[18:19], 0
	s_waitcnt vmcnt(0)
	v_cmp_gt_u32_e32 vcc, v1, v2
	s_and_saveexec_b64 s[14:15], vcc
	s_cbranch_execz .LBB0_1046
	s_add_u32 s12, s34, 0x4200
	s_addc_u32 s13, s35, 0
	s_mov_b32 s3, 1
	s_branch .LBB0_1039

; __device__ __forceinline__ unsigned xb_ld(unsigned* p)              { return __hip_atomic_load(p, __ATOMIC_RELAXED, __HIP_MEMORY_SCOPE_AGENT); }
; __device__ __forceinline__ unsigned xb_add(unsigned* p, unsigned v) { return __hip_atomic_fetch_add(p, v, __ATOMIC_RELAXED, __HIP_MEMORY_SCOPE_AGENT); }
; #define XB_SPIN(cond, bar) do { unsigned _sp = 0; while (cond) { __builtin_amdgcn_s_sleep(1); \
;     if ((++_sp & 255u) == 0u) { if (xb_ld(&(bar)[XB_TMO])) break; if (_sp > XB_SPIN_CAP) { atomicAdd(&(bar)[XB_TMO], 1u); break; } } } } while (0)
; __device__ __forceinline__ void xcd_barrier(const XcdBarrier& b) {
;     ...
;             const unsigned tg = og / nx;
;             if (og + 1u == (tg + 1u) * nx) xb_add(&bar[XB_TOPGEN], 1u);
;             else XB_SPIN(xb_ld(&bar[XB_TOPGEN]) == tg, bar);
.LBB0_1043:
	global_load_dword v2, v195, s[8:9] sc1
	s_add_i32 s3, s3, 1
	s_mov_b64 s[26:27], -1
	s_waitcnt vmcnt(0)
	v_cmp_ge_u32_e32 vcc, v2, v1
	s_orn2_b64 s[24:25], vcc, exec
	s_branch .LBB0_1038

; __device__ __forceinline__ unsigned xb_ld(unsigned* p)              { return __hip_atomic_load(p, __ATOMIC_RELAXED, __HIP_MEMORY_SCOPE_AGENT); }
; __device__ __forceinline__ unsigned xb_add(unsigned* p, unsigned v) { return __hip_atomic_fetch_add(p, v, __ATOMIC_RELAXED, __HIP_MEMORY_SCOPE_AGENT); }
; #define XB_SPIN(cond, bar) do { unsigned _sp = 0; while (cond) { __builtin_amdgcn_s_sleep(1); \
;     if ((++_sp & 255u) == 0u) { if (xb_ld(&(bar)[XB_TMO])) break; if (_sp > XB_SPIN_CAP) { atomicAdd(&(bar)[XB_TMO], 1u); break; } } } } while (0)
; __device__ __forceinline__ void xcd_barrier(const XcdBarrier& b) {
;     ...
;             if (og + 1u == (tg + 1u) * nx) xb_add(&bar[XB_TOPGEN], 1u);
;             else XB_SPIN(xb_ld(&bar[XB_TOPGEN]) == tg, bar);
;             __builtin_amdgcn_fence(__ATOMIC_ACQUIRE, "agent");
;             xb_add(&bar[XB_XGEN(b.x)], 1u);
.LBB0_1047:
	s_or_b64 exec, exec, s[10:11]
	s_and_saveexec_b64 s[8:9], s[12:13]
	s_cbranch_execz .LBB0_1049
.LBB0_1049:
	s_or_b64 exec, exec, s[8:9]
	s_mov_b64 s[8:9], exec
	v_mbcnt_lo_u32_b32 v1, s8, 0
	v_mbcnt_hi_u32_b32 v1, s9, v1
	v_cmp_eq_u32_e32 vcc, 0, v1
	s_waitcnt vmcnt(0)
	buffer_inv sc1
	s_and_saveexec_b64 s[10:11], vcc
	s_cbranch_execz .LBB0_1051
	s_bcnt1_i32_b64 s3, s[8:9]
	v_mov_b32_e32 v1, s3
	v_mov_b32_e32 v2, 0x2000

; __device__ __forceinline__ unsigned xb_ld(unsigned* p)              { return __hip_atomic_load(p, __ATOMIC_RELAXED, __HIP_MEMORY_SCOPE_AGENT); }
; __device__ __forceinline__ unsigned xb_add(unsigned* p, unsigned v) { return __hip_atomic_fetch_add(p, v, __ATOMIC_RELAXED, __HIP_MEMORY_SCOPE_AGENT); }
; #define XB_SPIN(cond, bar) do { unsigned _sp = 0; while (cond) { __builtin_amdgcn_s_sleep(1); \
;     if ((++_sp & 255u) == 0u) { if (xb_ld(&(bar)[XB_TMO])) break; if (_sp > XB_SPIN_CAP) { atomicAdd(&(bar)[XB_TMO], 1u); break; } } } } while (0)
; __device__ __forceinline__ void xcd_barrier(const XcdBarrier& b) {
;     ...
;             const unsigned og = xb_add(&bar[XB_TOP], 1u);
;             const unsigned tg = og / nx;
;             if (og + 1u == (tg + 1u) * nx) xb_add(&bar[XB_TOPGEN], 1u);
;             else XB_SPIN(xb_ld(&bar[XB_TOPGEN]) == tg, bar);
.LBB0_1079:
	s_or_b64 exec, exec, s[10:11]
	v_cvt_f32_u32_e32 v6, v4
	s_waitcnt vmcnt(0)
	v_readfirstlane_b32 s2, v5
	v_sub_u32_e32 v5, 0, v4
	v_rcp_iflag_f32_e32 v6, v6
	v_add_u32_e32 v7, s2, v3
	v_mul_f32_e32 v6, 0x4f7ffffe, v6
	v_cvt_u32_f32_e32 v6, v6
	v_mul_lo_u32 v3, v5, v6
	v_mul_hi_u32 v3, v6, v3
	v_add_u32_e32 v3, v6, v3
	v_mul_hi_u32 v3, v7, v3
	v_mul_lo_u32 v5, v3, v4
	v_sub_u32_e32 v5, v7, v5
	v_add_u32_e32 v6, 1, v3
	v_cmp_ge_u32_e32 vcc, v5, v4
	s_nop 1
	v_cndmask_b32_e32 v3, v3, v6, vcc
	v_sub_u32_e32 v6, v5, v4
	v_cndmask_b32_e32 v5, v5, v6, vcc
	v_add_u32_e32 v6, 1, v3
	v_cmp_ge_u32_e32 vcc, v5, v4
	v_add_u32_e32 v5, 1, v7
	s_nop 0
	v_cndmask_b32_e32 v3, v3, v6, vcc
	v_mul_lo_u32 v6, v4, v3
	v_add_u32_e32 v4, v6, v4
	v_cmp_ne_u32_e32 vcc, v5, v4
	s_and_saveexec_b64 s[8:9], vcc
	s_xor_b64 s[8:9], exec, s[8:9]
	s_cbranch_execz .LBB0_1093
	s_waitcnt lgkmcnt(0)
	v_mad_u32_u24 v3, v2, v3, v2
	s_add_u32 s14, s34, 0x7400
	s_addc_u32 s15, s35, 0
	v_mov_b32_e32 v2, 0
	global_load_dword v2, v2, s[14:15] sc1
	s_waitcnt vmcnt(0)
	v_cmp_gt_u32_e32 vcc, v3, v2
	s_and_saveexec_b64 s[10:11], vcc
	s_cbranch_execz .LBB0_1092
	s_add_u32 s12, s34, 0x4200
	s_addc_u32 s13, s35, 0
	s_mov_b32 s2, 1
	s_mov_b64 s[18:19], 0
	s_branch .LBB0_1083

; __device__ __forceinline__ unsigned xb_ld(unsigned* p)              { return __hip_atomic_load(p, __ATOMIC_RELAXED, __HIP_MEMORY_SCOPE_AGENT); }
; __device__ __forceinline__ unsigned xb_add(unsigned* p, unsigned v) { return __hip_atomic_fetch_add(p, v, __ATOMIC_RELAXED, __HIP_MEMORY_SCOPE_AGENT); }
; #define XB_SPIN(cond, bar) do { unsigned _sp = 0; while (cond) { __builtin_amdgcn_s_sleep(1); \
;     if ((++_sp & 255u) == 0u) { if (xb_ld(&(bar)[XB_TMO])) break; if (_sp > XB_SPIN_CAP) { atomicAdd(&(bar)[XB_TMO], 1u); break; } } } } while (0)
; __device__ __forceinline__ void xcd_barrier(const XcdBarrier& b) {
;     ...
;             const unsigned tg = og / nx;
;             if (og + 1u == (tg + 1u) * nx) xb_add(&bar[XB_TOPGEN], 1u);
;             else XB_SPIN(xb_ld(&bar[XB_TOPGEN]) == tg, bar);
.LBB0_1087:
	global_load_dword v2, v195, s[14:15] sc1
	s_add_i32 s2, s2, 1
	s_mov_b64 s[24:25], -1
	s_waitcnt vmcnt(0)
	v_cmp_ge_u32_e32 vcc, v2, v3
	s_orn2_b64 s[22:23], vcc, exec
	s_branch .LBB0_1082

; __device__ __forceinline__ unsigned xb_ld(unsigned* p)              { return __hip_atomic_load(p, __ATOMIC_RELAXED, __HIP_MEMORY_SCOPE_AGENT); }
; __device__ __forceinline__ unsigned xb_add(unsigned* p, unsigned v) { return __hip_atomic_fetch_add(p, v, __ATOMIC_RELAXED, __HIP_MEMORY_SCOPE_AGENT); }
; #define XB_SPIN(cond, bar) do { unsigned _sp = 0; while (cond) { __builtin_amdgcn_s_sleep(1); \
;     if ((++_sp & 255u) == 0u) { if (xb_ld(&(bar)[XB_TMO])) break; if (_sp > XB_SPIN_CAP) { atomicAdd(&(bar)[XB_TMO], 1u); break; } } } } while (0)
; __device__ __forceinline__ void xcd_barrier(const XcdBarrier& b) {
;     ...
;             const unsigned og = xb_add(&bar[XB_TOP], 1u);
;             const unsigned tg = og / nx;
;             if (og + 1u == (tg + 1u) * nx) xb_add(&bar[XB_TOPGEN], 1u);
;             else XB_SPIN(xb_ld(&bar[XB_TOPGEN]) == tg, bar);
.LBB0_1096:
	s_or_b64 exec, exec, s[10:11]
	s_waitcnt vmcnt(0)
	v_readfirstlane_b32 s2, v4
	v_cvt_f32_u32_e32 v4, v2
	v_sub_u32_e32 v5, 0, v2
	v_add_u32_e32 v3, s2, v3
	s_add_u32 s8, s34, 0x7400
	v_rcp_iflag_f32_e32 v4, v4
	s_addc_u32 s9, s35, 0
	s_mov_b64 s[12:13], -1
	v_mul_f32_e32 v4, 0x4f7ffffe, v4
	v_cvt_u32_f32_e32 v4, v4
	v_mul_lo_u32 v5, v5, v4
	v_mul_hi_u32 v5, v4, v5
	v_add_u32_e32 v4, v4, v5
	v_mul_hi_u32 v4, v3, v4
	v_mul_lo_u32 v5, v4, v2
	v_sub_u32_e32 v5, v3, v5
	v_cmp_ge_u32_e32 vcc, v5, v2
	v_add_u32_e32 v6, 1, v4
	v_add_u32_e32 v3, 1, v3
	v_cndmask_b32_e32 v4, v4, v6, vcc
	v_sub_u32_e32 v6, v5, v2
	v_cndmask_b32_e32 v5, v5, v6, vcc
	v_cmp_ge_u32_e32 vcc, v5, v2
	v_add_u32_e32 v5, 1, v4
	s_nop 0
	v_cndmask_b32_e32 v4, v4, v5, vcc
	v_mul_lo_u32 v5, v2, v4
	v_add_u32_e32 v2, v5, v2
	v_cmp_ne_u32_e32 vcc, v3, v2
	v_mov_b32_e32 v4, v2
	v_mov_b64_e32 v[2:3], s[8:9]
	s_and_saveexec_b64 s[10:11], vcc
	s_cbranch_execz .LBB0_1108
	global_load_dword v2, v195, s[8:9] sc1
	s_mov_b64 s[18:19], 0
	s_waitcnt vmcnt(0)
	v_cmp_gt_u32_e32 vcc, v4, v2
	s_and_saveexec_b64 s[14:15], vcc
	s_cbranch_execz .LBB0_1107
	s_add_u32 s12, s34, 0x4200
	s_addc_u32 s13, s35, 0
	s_mov_b32 s2, 1
	s_branch .LBB0_1100

; __device__ __forceinline__ unsigned xb_ld(unsigned* p)              { return __hip_atomic_load(p, __ATOMIC_RELAXED, __HIP_MEMORY_SCOPE_AGENT); }
; __device__ __forceinline__ unsigned xb_add(unsigned* p, unsigned v) { return __hip_atomic_fetch_add(p, v, __ATOMIC_RELAXED, __HIP_MEMORY_SCOPE_AGENT); }
; #define XB_SPIN(cond, bar) do { unsigned _sp = 0; while (cond) { __builtin_amdgcn_s_sleep(1); \
;     if ((++_sp & 255u) == 0u) { if (xb_ld(&(bar)[XB_TMO])) break; if (_sp > XB_SPIN_CAP) { atomicAdd(&(bar)[XB_TMO], 1u); break; } } } } while (0)
; __device__ __forceinline__ void xcd_barrier(const XcdBarrier& b) {
;     ...
;             const unsigned tg = og / nx;
;             if (og + 1u == (tg + 1u) * nx) xb_add(&bar[XB_TOPGEN], 1u);
;             else XB_SPIN(xb_ld(&bar[XB_TOPGEN]) == tg, bar);
.LBB0_1104:
	global_load_dword v2, v195, s[8:9] sc1
	s_add_i32 s2, s2, 1
	s_mov_b64 s[24:25], -1
	s_waitcnt vmcnt(0)
	v_cmp_ge_u32_e32 vcc, v2, v4
	s_orn2_b64 s[22:23], vcc, exec
	s_branch .LBB0_1099

; __device__ __forceinline__ unsigned xb_ld(unsigned* p)              { return __hip_atomic_load(p, __ATOMIC_RELAXED, __HIP_MEMORY_SCOPE_AGENT); }
; __device__ __forceinline__ unsigned xb_add(unsigned* p, unsigned v) { return __hip_atomic_fetch_add(p, v, __ATOMIC_RELAXED, __HIP_MEMORY_SCOPE_AGENT); }
; #define XB_SPIN(cond, bar) do { unsigned _sp = 0; while (cond) { __builtin_amdgcn_s_sleep(1); \
;     if ((++_sp & 255u) == 0u) { if (xb_ld(&(bar)[XB_TMO])) break; if (_sp > XB_SPIN_CAP) { atomicAdd(&(bar)[XB_TMO], 1u); break; } } } } while (0)
; __device__ __forceinline__ void xcd_barrier(const XcdBarrier& b) {
;     ...
;             if (og + 1u == (tg + 1u) * nx) xb_add(&bar[XB_TOPGEN], 1u);
;             else XB_SPIN(xb_ld(&bar[XB_TOPGEN]) == tg, bar);
;             __builtin_amdgcn_fence(__ATOMIC_ACQUIRE, "agent");
;             xb_add(&bar[XB_XGEN(b.x)], 1u);
.LBB0_1108:
	s_or_b64 exec, exec, s[10:11]
	s_and_saveexec_b64 s[8:9], s[12:13]
	s_cbranch_execz .LBB0_1110
.LBB0_1110:
	s_or_b64 exec, exec, s[8:9]
	s_mov_b64 s[8:9], exec
	v_mbcnt_lo_u32_b32 v2, s8, 0
	v_mbcnt_hi_u32_b32 v2, s9, v2
	v_cmp_eq_u32_e32 vcc, 0, v2
	s_waitcnt vmcnt(0)
	buffer_inv sc1
	s_and_saveexec_b64 s[10:11], vcc
	s_cbranch_execz .LBB0_1112
	s_bcnt1_i32_b64 s2, s[8:9]
	v_mov_b32_e32 v2, s2
	v_mov_b32_e32 v3, 0x2000

; __device__ __forceinline__ unsigned xb_ld(unsigned* p)              { return __hip_atomic_load(p, __ATOMIC_RELAXED, __HIP_MEMORY_SCOPE_AGENT); }
; __device__ __forceinline__ unsigned xb_add(unsigned* p, unsigned v) { return __hip_atomic_fetch_add(p, v, __ATOMIC_RELAXED, __HIP_MEMORY_SCOPE_AGENT); }
; #define XB_SPIN(cond, bar) do { unsigned _sp = 0; while (cond) { __builtin_amdgcn_s_sleep(1); \
;     if ((++_sp & 255u) == 0u) { if (xb_ld(&(bar)[XB_TMO])) break; if (_sp > XB_SPIN_CAP) { atomicAdd(&(bar)[XB_TMO], 1u); break; } } } } while (0)
; __device__ __forceinline__ void xcd_barrier(const XcdBarrier& b) {
;     ...
;             const unsigned og = xb_add(&bar[XB_TOP], 1u);
;             const unsigned tg = og / nx;
;             if (og + 1u == (tg + 1u) * nx) xb_add(&bar[XB_TOPGEN], 1u);
;             else XB_SPIN(xb_ld(&bar[XB_TOPGEN]) == tg, bar);
.LBB0_1152:
	s_or_b64 exec, exec, s[10:11]
	v_cvt_f32_u32_e32 v6, v4
	s_waitcnt vmcnt(0)
	v_readfirstlane_b32 s2, v5
	v_sub_u32_e32 v5, 0, v4
	v_rcp_iflag_f32_e32 v6, v6
	v_add_u32_e32 v7, s2, v3
	v_mul_f32_e32 v6, 0x4f7ffffe, v6
	v_cvt_u32_f32_e32 v6, v6
	v_mul_lo_u32 v3, v5, v6
	v_mul_hi_u32 v3, v6, v3
	v_add_u32_e32 v3, v6, v3
	v_mul_hi_u32 v3, v7, v3
	v_mul_lo_u32 v5, v3, v4
	v_sub_u32_e32 v5, v7, v5
	v_add_u32_e32 v6, 1, v3
	v_cmp_ge_u32_e32 vcc, v5, v4
	s_nop 1
	v_cndmask_b32_e32 v3, v3, v6, vcc
	v_sub_u32_e32 v6, v5, v4
	v_cndmask_b32_e32 v5, v5, v6, vcc
	v_add_u32_e32 v6, 1, v3
	v_cmp_ge_u32_e32 vcc, v5, v4
	v_add_u32_e32 v5, 1, v7
	s_nop 0
	v_cndmask_b32_e32 v3, v3, v6, vcc
	v_mul_lo_u32 v6, v4, v3
	v_add_u32_e32 v4, v6, v4
	v_cmp_ne_u32_e32 vcc, v5, v4
	s_and_saveexec_b64 s[8:9], vcc
	s_xor_b64 s[8:9], exec, s[8:9]
	s_cbranch_execz .LBB0_1166
	s_waitcnt lgkmcnt(0)
	v_mad_u32_u24 v3, v2, v3, v2
	s_add_u32 s14, s34, 0x7400
	s_addc_u32 s15, s35, 0
	v_mov_b32_e32 v2, 0
	global_load_dword v2, v2, s[14:15] sc1
	s_waitcnt vmcnt(0)
	v_cmp_gt_u32_e32 vcc, v3, v2
	s_and_saveexec_b64 s[10:11], vcc
	s_cbranch_execz .LBB0_1165
	s_add_u32 s12, s34, 0x4200
	s_addc_u32 s13, s35, 0
	s_mov_b32 s2, 1
	s_mov_b64 s[16:17], 0
	s_branch .LBB0_1156

; __device__ __forceinline__ unsigned xb_ld(unsigned* p)              { return __hip_atomic_load(p, __ATOMIC_RELAXED, __HIP_MEMORY_SCOPE_AGENT); }
; __device__ __forceinline__ unsigned xb_add(unsigned* p, unsigned v) { return __hip_atomic_fetch_add(p, v, __ATOMIC_RELAXED, __HIP_MEMORY_SCOPE_AGENT); }
; #define XB_SPIN(cond, bar) do { unsigned _sp = 0; while (cond) { __builtin_amdgcn_s_sleep(1); \
;     if ((++_sp & 255u) == 0u) { if (xb_ld(&(bar)[XB_TMO])) break; if (_sp > XB_SPIN_CAP) { atomicAdd(&(bar)[XB_TMO], 1u); break; } } } } while (0)
; __device__ __forceinline__ void xcd_barrier(const XcdBarrier& b) {
;     ...
;             const unsigned tg = og / nx;
;             if (og + 1u == (tg + 1u) * nx) xb_add(&bar[XB_TOPGEN], 1u);
;             else XB_SPIN(xb_ld(&bar[XB_TOPGEN]) == tg, bar);
.LBB0_1160:
	global_load_dword v2, v195, s[14:15] sc1
	s_add_i32 s2, s2, 1
	s_mov_b64 s[22:23], -1
	s_waitcnt vmcnt(0)
	v_cmp_ge_u32_e32 vcc, v2, v3
	s_orn2_b64 s[20:21], vcc, exec
	s_branch .LBB0_1155

; __device__ __forceinline__ unsigned xb_ld(unsigned* p)              { return __hip_atomic_load(p, __ATOMIC_RELAXED, __HIP_MEMORY_SCOPE_AGENT); }
; __device__ __forceinline__ unsigned xb_add(unsigned* p, unsigned v) { return __hip_atomic_fetch_add(p, v, __ATOMIC_RELAXED, __HIP_MEMORY_SCOPE_AGENT); }
; #define XB_SPIN(cond, bar) do { unsigned _sp = 0; while (cond) { __builtin_amdgcn_s_sleep(1); \
;     if ((++_sp & 255u) == 0u) { if (xb_ld(&(bar)[XB_TMO])) break; if (_sp > XB_SPIN_CAP) { atomicAdd(&(bar)[XB_TMO], 1u); break; } } } } while (0)
; __device__ __forceinline__ void xcd_barrier(const XcdBarrier& b) {
;     ...
;             const unsigned og = xb_add(&bar[XB_TOP], 1u);
;             const unsigned tg = og / nx;
;             if (og + 1u == (tg + 1u) * nx) xb_add(&bar[XB_TOPGEN], 1u);
;             else XB_SPIN(xb_ld(&bar[XB_TOPGEN]) == tg, bar);
.LBB0_1169:
	s_or_b64 exec, exec, s[10:11]
	s_waitcnt vmcnt(0)
	v_readfirstlane_b32 s2, v4
	v_cvt_f32_u32_e32 v4, v2
	v_sub_u32_e32 v5, 0, v2
	v_add_u32_e32 v3, s2, v3
	s_add_u32 s8, s34, 0x7400
	v_rcp_iflag_f32_e32 v4, v4
	s_addc_u32 s9, s35, 0
	s_mov_b64 s[12:13], -1
	v_mul_f32_e32 v4, 0x4f7ffffe, v4
	v_cvt_u32_f32_e32 v4, v4
	v_mul_lo_u32 v5, v5, v4
	v_mul_hi_u32 v5, v4, v5
	v_add_u32_e32 v4, v4, v5
	v_mul_hi_u32 v4, v3, v4
	v_mul_lo_u32 v5, v4, v2
	v_sub_u32_e32 v5, v3, v5
	v_cmp_ge_u32_e32 vcc, v5, v2
	v_add_u32_e32 v6, 1, v4
	v_add_u32_e32 v3, 1, v3
	v_cndmask_b32_e32 v4, v4, v6, vcc
	v_sub_u32_e32 v6, v5, v2
	v_cndmask_b32_e32 v5, v5, v6, vcc
	v_cmp_ge_u32_e32 vcc, v5, v2
	v_add_u32_e32 v5, 1, v4
	s_nop 0
	v_cndmask_b32_e32 v4, v4, v5, vcc
	v_mul_lo_u32 v5, v2, v4
	v_add_u32_e32 v2, v5, v2
	v_cmp_ne_u32_e32 vcc, v3, v2
	v_mov_b32_e32 v4, v2
	v_mov_b64_e32 v[2:3], s[8:9]
	s_and_saveexec_b64 s[10:11], vcc
	s_cbranch_execz .LBB0_1181
	global_load_dword v2, v195, s[8:9] sc1
	s_mov_b64 s[16:17], 0
	s_waitcnt vmcnt(0)
	v_cmp_gt_u32_e32 vcc, v4, v2
	s_and_saveexec_b64 s[14:15], vcc
	s_cbranch_execz .LBB0_1180
	s_add_u32 s12, s34, 0x4200
	s_addc_u32 s13, s35, 0
	s_mov_b32 s2, 1
	s_branch .LBB0_1173

; __device__ __forceinline__ unsigned xb_ld(unsigned* p)              { return __hip_atomic_load(p, __ATOMIC_RELAXED, __HIP_MEMORY_SCOPE_AGENT); }
; __device__ __forceinline__ unsigned xb_add(unsigned* p, unsigned v) { return __hip_atomic_fetch_add(p, v, __ATOMIC_RELAXED, __HIP_MEMORY_SCOPE_AGENT); }
; #define XB_SPIN(cond, bar) do { unsigned _sp = 0; while (cond) { __builtin_amdgcn_s_sleep(1); \
;     if ((++_sp & 255u) == 0u) { if (xb_ld(&(bar)[XB_TMO])) break; if (_sp > XB_SPIN_CAP) { atomicAdd(&(bar)[XB_TMO], 1u); break; } } } } while (0)
; __device__ __forceinline__ void xcd_barrier(const XcdBarrier& b) {
;     ...
;             const unsigned tg = og / nx;
;             if (og + 1u == (tg + 1u) * nx) xb_add(&bar[XB_TOPGEN], 1u);
;             else XB_SPIN(xb_ld(&bar[XB_TOPGEN]) == tg, bar);
.LBB0_1177:
	global_load_dword v2, v195, s[8:9] sc1
	s_add_i32 s2, s2, 1
	s_mov_b64 s[22:23], -1
	s_waitcnt vmcnt(0)
	v_cmp_ge_u32_e32 vcc, v2, v4
	s_orn2_b64 s[20:21], vcc, exec
	s_branch .LBB0_1172

; __device__ __forceinline__ unsigned xb_ld(unsigned* p)              { return __hip_atomic_load(p, __ATOMIC_RELAXED, __HIP_MEMORY_SCOPE_AGENT); }
; __device__ __forceinline__ unsigned xb_add(unsigned* p, unsigned v) { return __hip_atomic_fetch_add(p, v, __ATOMIC_RELAXED, __HIP_MEMORY_SCOPE_AGENT); }
; #define XB_SPIN(cond, bar) do { unsigned _sp = 0; while (cond) { __builtin_amdgcn_s_sleep(1); \
;     if ((++_sp & 255u) == 0u) { if (xb_ld(&(bar)[XB_TMO])) break; if (_sp > XB_SPIN_CAP) { atomicAdd(&(bar)[XB_TMO], 1u); break; } } } } while (0)
; __device__ __forceinline__ void xcd_barrier(const XcdBarrier& b) {
;     ...
;             if (og + 1u == (tg + 1u) * nx) xb_add(&bar[XB_TOPGEN], 1u);
;             else XB_SPIN(xb_ld(&bar[XB_TOPGEN]) == tg, bar);
;             __builtin_amdgcn_fence(__ATOMIC_ACQUIRE, "agent");
;             xb_add(&bar[XB_XGEN(b.x)], 1u);
.LBB0_1181:
	s_or_b64 exec, exec, s[10:11]
	s_and_saveexec_b64 s[8:9], s[12:13]
	s_cbranch_execz .LBB0_1183
.LBB0_1183:
	s_or_b64 exec, exec, s[8:9]
	s_mov_b64 s[8:9], exec
	v_mbcnt_lo_u32_b32 v2, s8, 0
	v_mbcnt_hi_u32_b32 v2, s9, v2
	v_cmp_eq_u32_e32 vcc, 0, v2
	s_waitcnt vmcnt(0)
	buffer_inv sc1
	s_and_saveexec_b64 s[10:11], vcc
	s_cbranch_execz .LBB0_1185
	s_bcnt1_i32_b64 s2, s[8:9]
	v_mov_b32_e32 v2, s2
	v_mov_b32_e32 v3, 0x2000

; __device__ __forceinline__ unsigned xb_ld(unsigned* p)              { return __hip_atomic_load(p, __ATOMIC_RELAXED, __HIP_MEMORY_SCOPE_AGENT); }
; __device__ __forceinline__ unsigned xb_add(unsigned* p, unsigned v) { return __hip_atomic_fetch_add(p, v, __ATOMIC_RELAXED, __HIP_MEMORY_SCOPE_AGENT); }
; #define XB_SPIN(cond, bar) do { unsigned _sp = 0; while (cond) { __builtin_amdgcn_s_sleep(1); \
;     if ((++_sp & 255u) == 0u) { if (xb_ld(&(bar)[XB_TMO])) break; if (_sp > XB_SPIN_CAP) { atomicAdd(&(bar)[XB_TMO], 1u); break; } } } } while (0)
; __device__ __forceinline__ void xcd_barrier(const XcdBarrier& b) {
;     ...
;             if (og + 1u == (tg + 1u) * nx) xb_add(&bar[XB_TOPGEN], 1u);
;             else XB_SPIN(xb_ld(&bar[XB_TOPGEN]) == tg, bar);
;             __builtin_amdgcn_fence(__ATOMIC_ACQUIRE, "agent");
;             xb_add(&bar[XB_XGEN(b.x)], 1u);
.LBB0_1261:
	s_or_b64 exec, exec, s[10:11]
	s_and_saveexec_b64 s[8:9], s[12:13]
	s_cbranch_execz .LBB0_1263
.LBB0_1263:
	s_or_b64 exec, exec, s[8:9]
	s_mov_b64 s[8:9], exec
	v_mbcnt_lo_u32_b32 v2, s8, 0
	v_mbcnt_hi_u32_b32 v2, s9, v2
	v_cmp_eq_u32_e32 vcc, 0, v2
	s_waitcnt vmcnt(0)
	buffer_inv sc1
	s_and_saveexec_b64 s[10:11], vcc
	s_cbranch_execz .LBB0_1265
	s_bcnt1_i32_b64 s2, s[8:9]
	v_mov_b32_e32 v2, s2
	v_mov_b32_e32 v3, 0x2000

; __device__ __forceinline__ unsigned xb_ld(unsigned* p)              { return __hip_atomic_load(p, __ATOMIC_RELAXED, __HIP_MEMORY_SCOPE_AGENT); }
; __device__ __forceinline__ unsigned xb_add(unsigned* p, unsigned v) { return __hip_atomic_fetch_add(p, v, __ATOMIC_RELAXED, __HIP_MEMORY_SCOPE_AGENT); }
; #define XB_SPIN(cond, bar) do { unsigned _sp = 0; while (cond) { __builtin_amdgcn_s_sleep(1); \
;     if ((++_sp & 255u) == 0u) { if (xb_ld(&(bar)[XB_TMO])) break; if (_sp > XB_SPIN_CAP) { atomicAdd(&(bar)[XB_TMO], 1u); break; } } } } while (0)
; __device__ __forceinline__ void xcd_barrier(const XcdBarrier& b) {
;     ...
;             const unsigned og = xb_add(&bar[XB_TOP], 1u);
;             const unsigned tg = og / nx;
;             if (og + 1u == (tg + 1u) * nx) xb_add(&bar[XB_TOPGEN], 1u);
;             else XB_SPIN(xb_ld(&bar[XB_TOPGEN]) == tg, bar);
.LBB0_1349:
	s_or_b64 exec, exec, s[10:11]
	v_cvt_f32_u32_e32 v5, v3
	s_waitcnt vmcnt(0)
	v_readfirstlane_b32 s3, v4
	v_sub_u32_e32 v4, 0, v3
	v_rcp_iflag_f32_e32 v5, v5
	v_add_u32_e32 v6, s3, v1
	v_mul_f32_e32 v5, 0x4f7ffffe, v5
	v_cvt_u32_f32_e32 v5, v5
	v_mul_lo_u32 v1, v4, v5
	v_mul_hi_u32 v1, v5, v1
	v_add_u32_e32 v1, v5, v1
	v_mul_hi_u32 v1, v6, v1
	v_mul_lo_u32 v4, v1, v3
	v_sub_u32_e32 v4, v6, v4
	v_add_u32_e32 v5, 1, v1
	v_cmp_ge_u32_e32 vcc, v4, v3
	s_nop 1
	v_cndmask_b32_e32 v1, v1, v5, vcc
	v_sub_u32_e32 v5, v4, v3
	v_cndmask_b32_e32 v4, v4, v5, vcc
	v_add_u32_e32 v5, 1, v1
	v_cmp_ge_u32_e32 vcc, v4, v3
	v_add_u32_e32 v4, 1, v6
	s_nop 0
	v_cndmask_b32_e32 v1, v1, v5, vcc
	v_mul_lo_u32 v5, v3, v1
	v_add_u32_e32 v3, v5, v3
	v_cmp_ne_u32_e32 vcc, v4, v3
	s_and_saveexec_b64 s[8:9], vcc
	s_xor_b64 s[8:9], exec, s[8:9]
	s_cbranch_execz .LBB0_1363
	s_waitcnt lgkmcnt(0)
	v_mad_u32_u24 v1, v2, v1, v2
	s_add_u32 s14, s34, 0x7400
	s_addc_u32 s15, s35, 0
	v_mov_b32_e32 v2, 0
	global_load_dword v2, v2, s[14:15] sc1
	s_waitcnt vmcnt(0)
	v_cmp_gt_u32_e32 vcc, v1, v2
	s_and_saveexec_b64 s[10:11], vcc
	s_cbranch_execz .LBB0_1362
	s_add_u32 s12, s34, 0x4200
	s_addc_u32 s13, s35, 0
	s_mov_b32 s3, 1
	s_mov_b64 s[16:17], 0
	s_branch .LBB0_1353

; __device__ __forceinline__ unsigned xb_ld(unsigned* p)              { return __hip_atomic_load(p, __ATOMIC_RELAXED, __HIP_MEMORY_SCOPE_AGENT); }
; __device__ __forceinline__ unsigned xb_add(unsigned* p, unsigned v) { return __hip_atomic_fetch_add(p, v, __ATOMIC_RELAXED, __HIP_MEMORY_SCOPE_AGENT); }
; #define XB_SPIN(cond, bar) do { unsigned _sp = 0; while (cond) { __builtin_amdgcn_s_sleep(1); \
;     if ((++_sp & 255u) == 0u) { if (xb_ld(&(bar)[XB_TMO])) break; if (_sp > XB_SPIN_CAP) { atomicAdd(&(bar)[XB_TMO], 1u); break; } } } } while (0)
; __device__ __forceinline__ void xcd_barrier(const XcdBarrier& b) {
;     ...
;             const unsigned tg = og / nx;
;             if (og + 1u == (tg + 1u) * nx) xb_add(&bar[XB_TOPGEN], 1u);
;             else XB_SPIN(xb_ld(&bar[XB_TOPGEN]) == tg, bar);
.LBB0_1357:
	global_load_dword v2, v195, s[14:15] sc1
	s_add_i32 s3, s3, 1
	s_mov_b64 s[22:23], -1
	s_waitcnt vmcnt(0)
	v_cmp_ge_u32_e32 vcc, v2, v1
	s_orn2_b64 s[20:21], vcc, exec
	s_branch .LBB0_1352

; __device__ __forceinline__ unsigned xb_ld(unsigned* p)              { return __hip_atomic_load(p, __ATOMIC_RELAXED, __HIP_MEMORY_SCOPE_AGENT); }
; __device__ __forceinline__ unsigned xb_add(unsigned* p, unsigned v) { return __hip_atomic_fetch_add(p, v, __ATOMIC_RELAXED, __HIP_MEMORY_SCOPE_AGENT); }
; #define XB_SPIN(cond, bar) do { unsigned _sp = 0; while (cond) { __builtin_amdgcn_s_sleep(1); \
;     if ((++_sp & 255u) == 0u) { if (xb_ld(&(bar)[XB_TMO])) break; if (_sp > XB_SPIN_CAP) { atomicAdd(&(bar)[XB_TMO], 1u); break; } } } } while (0)
; __device__ __forceinline__ void xcd_barrier(const XcdBarrier& b) {
;     ...
;             const unsigned og = xb_add(&bar[XB_TOP], 1u);
;             const unsigned tg = og / nx;
;             if (og + 1u == (tg + 1u) * nx) xb_add(&bar[XB_TOPGEN], 1u);
;             else XB_SPIN(xb_ld(&bar[XB_TOPGEN]) == tg, bar);
.LBB0_1366:
	s_or_b64 exec, exec, s[10:11]
	s_waitcnt vmcnt(0)
	v_readfirstlane_b32 s3, v3
	v_sub_u32_e32 v4, 0, v2
	s_add_u32 s8, s34, 0x7400
	v_add_u32_e32 v3, s3, v1
	v_cvt_f32_u32_e32 v1, v2
	s_addc_u32 s9, s35, 0
	s_mov_b64 s[12:13], -1
	v_rcp_iflag_f32_e32 v1, v1
	s_nop 0
	v_mul_f32_e32 v1, 0x4f7ffffe, v1
	v_cvt_u32_f32_e32 v1, v1
	v_mul_lo_u32 v4, v4, v1
	v_mul_hi_u32 v4, v1, v4
	v_add_u32_e32 v1, v1, v4
	v_mul_hi_u32 v1, v3, v1
	v_mul_lo_u32 v4, v1, v2
	v_sub_u32_e32 v4, v3, v4
	v_cmp_ge_u32_e32 vcc, v4, v2
	v_add_u32_e32 v5, 1, v1
	v_add_u32_e32 v3, 1, v3
	v_cndmask_b32_e32 v1, v1, v5, vcc
	v_sub_u32_e32 v5, v4, v2
	v_cndmask_b32_e32 v4, v4, v5, vcc
	v_cmp_ge_u32_e32 vcc, v4, v2
	v_add_u32_e32 v4, 1, v1
	s_nop 0
	v_cndmask_b32_e32 v1, v1, v4, vcc
	v_mul_lo_u32 v4, v2, v1
	v_add_u32_e32 v2, v4, v2
	v_cmp_ne_u32_e32 vcc, v3, v2
	v_mov_b32_e32 v1, v2
	v_mov_b64_e32 v[2:3], s[8:9]
	s_and_saveexec_b64 s[10:11], vcc
	s_cbranch_execz .LBB0_1378
	global_load_dword v2, v195, s[8:9] sc1
	s_mov_b64 s[16:17], 0
	s_waitcnt vmcnt(0)
	v_cmp_gt_u32_e32 vcc, v1, v2
	s_and_saveexec_b64 s[14:15], vcc
	s_cbranch_execz .LBB0_1377
	s_add_u32 s12, s34, 0x4200
	s_addc_u32 s13, s35, 0
	s_mov_b32 s3, 1
	s_branch .LBB0_1370

; __device__ __forceinline__ unsigned xb_ld(unsigned* p)              { return __hip_atomic_load(p, __ATOMIC_RELAXED, __HIP_MEMORY_SCOPE_AGENT); }
; __device__ __forceinline__ unsigned xb_add(unsigned* p, unsigned v) { return __hip_atomic_fetch_add(p, v, __ATOMIC_RELAXED, __HIP_MEMORY_SCOPE_AGENT); }
; #define XB_SPIN(cond, bar) do { unsigned _sp = 0; while (cond) { __builtin_amdgcn_s_sleep(1); \
;     if ((++_sp & 255u) == 0u) { if (xb_ld(&(bar)[XB_TMO])) break; if (_sp > XB_SPIN_CAP) { atomicAdd(&(bar)[XB_TMO], 1u); break; } } } } while (0)
; __device__ __forceinline__ void xcd_barrier(const XcdBarrier& b) {
;     ...
;             const unsigned tg = og / nx;
;             if (og + 1u == (tg + 1u) * nx) xb_add(&bar[XB_TOPGEN], 1u);
;             else XB_SPIN(xb_ld(&bar[XB_TOPGEN]) == tg, bar);
.LBB0_1374:
	global_load_dword v2, v195, s[8:9] sc1
	s_add_i32 s3, s3, 1
	s_mov_b64 s[22:23], -1
	s_waitcnt vmcnt(0)
	v_cmp_ge_u32_e32 vcc, v2, v1
	s_orn2_b64 s[20:21], vcc, exec
	s_branch .LBB0_1369

; __device__ __forceinline__ unsigned xb_ld(unsigned* p)              { return __hip_atomic_load(p, __ATOMIC_RELAXED, __HIP_MEMORY_SCOPE_AGENT); }
; __device__ __forceinline__ unsigned xb_add(unsigned* p, unsigned v) { return __hip_atomic_fetch_add(p, v, __ATOMIC_RELAXED, __HIP_MEMORY_SCOPE_AGENT); }
; #define XB_SPIN(cond, bar) do { unsigned _sp = 0; while (cond) { __builtin_amdgcn_s_sleep(1); \
;     if ((++_sp & 255u) == 0u) { if (xb_ld(&(bar)[XB_TMO])) break; if (_sp > XB_SPIN_CAP) { atomicAdd(&(bar)[XB_TMO], 1u); break; } } } } while (0)
; __device__ __forceinline__ void xcd_barrier(const XcdBarrier& b) {
;     ...
;             if (og + 1u == (tg + 1u) * nx) xb_add(&bar[XB_TOPGEN], 1u);
;             else XB_SPIN(xb_ld(&bar[XB_TOPGEN]) == tg, bar);
;             __builtin_amdgcn_fence(__ATOMIC_ACQUIRE, "agent");
;             xb_add(&bar[XB_XGEN(b.x)], 1u);
.LBB0_1378:
	s_or_b64 exec, exec, s[10:11]
	s_and_saveexec_b64 s[8:9], s[12:13]
	s_cbranch_execz .LBB0_1380
.LBB0_1380:
	s_or_b64 exec, exec, s[8:9]
	s_mov_b64 s[8:9], exec
	v_mbcnt_lo_u32_b32 v1, s8, 0
	v_mbcnt_hi_u32_b32 v1, s9, v1
	v_cmp_eq_u32_e32 vcc, 0, v1
	s_waitcnt vmcnt(0)
	buffer_inv sc1
	s_and_saveexec_b64 s[10:11], vcc
	s_cbranch_execz .LBB0_1382
	s_bcnt1_i32_b64 s3, s[8:9]
	v_mov_b32_e32 v1, s3
	v_mov_b32_e32 v2, 0x2000

; __device__ __forceinline__ unsigned xb_ld(unsigned* p)              { return __hip_atomic_load(p, __ATOMIC_RELAXED, __HIP_MEMORY_SCOPE_AGENT); }
; __device__ __forceinline__ unsigned xb_add(unsigned* p, unsigned v) { return __hip_atomic_fetch_add(p, v, __ATOMIC_RELAXED, __HIP_MEMORY_SCOPE_AGENT); }
; #define XB_SPIN(cond, bar) do { unsigned _sp = 0; while (cond) { __builtin_amdgcn_s_sleep(1); \
;     if ((++_sp & 255u) == 0u) { if (xb_ld(&(bar)[XB_TMO])) break; if (_sp > XB_SPIN_CAP) { atomicAdd(&(bar)[XB_TMO], 1u); break; } } } } while (0)
; __device__ __forceinline__ void xcd_barrier(const XcdBarrier& b) {
;     ...
;             const unsigned og = xb_add(&bar[XB_TOP], 1u);
;             const unsigned tg = og / nx;
;             if (og + 1u == (tg + 1u) * nx) xb_add(&bar[XB_TOPGEN], 1u);
;             else XB_SPIN(xb_ld(&bar[XB_TOPGEN]) == tg, bar);
.LBB0_1427:
	s_or_b64 exec, exec, s[10:11]
	v_cvt_f32_u32_e32 v5, v3
	s_waitcnt vmcnt(0)
	v_readfirstlane_b32 s8, v4
	v_sub_u32_e32 v4, 0, v3
	v_rcp_iflag_f32_e32 v5, v5
	v_add_u32_e32 v6, s8, v1
	v_mul_f32_e32 v5, 0x4f7ffffe, v5
	v_cvt_u32_f32_e32 v5, v5
	v_mul_lo_u32 v1, v4, v5
	v_mul_hi_u32 v1, v5, v1
	v_add_u32_e32 v1, v5, v1
	v_mul_hi_u32 v1, v6, v1
	v_mul_lo_u32 v4, v1, v3
	v_sub_u32_e32 v4, v6, v4
	v_add_u32_e32 v5, 1, v1
	v_cmp_ge_u32_e32 vcc, v4, v3
	s_nop 1
	v_cndmask_b32_e32 v1, v1, v5, vcc
	v_sub_u32_e32 v5, v4, v3
	v_cndmask_b32_e32 v4, v4, v5, vcc
	v_add_u32_e32 v5, 1, v1
	v_cmp_ge_u32_e32 vcc, v4, v3
	v_add_u32_e32 v4, 1, v6
	s_nop 0
	v_cndmask_b32_e32 v1, v1, v5, vcc
	v_mul_lo_u32 v5, v3, v1
	v_add_u32_e32 v3, v5, v3
	v_cmp_ne_u32_e32 vcc, v4, v3
	s_and_saveexec_b64 s[8:9], vcc
	s_xor_b64 s[8:9], exec, s[8:9]
	s_cbranch_execz .LBB0_1441
	s_waitcnt lgkmcnt(0)
	v_mad_u32_u24 v1, v2, v1, v2
	s_add_u32 s14, s34, 0x7400
	s_addc_u32 s15, s35, 0
	v_mov_b32_e32 v2, 0
	global_load_dword v2, v2, s[14:15] sc1
	s_waitcnt vmcnt(0)
	v_cmp_gt_u32_e32 vcc, v1, v2
	s_and_saveexec_b64 s[10:11], vcc
	s_cbranch_execz .LBB0_1440
	s_add_u32 s12, s34, 0x4200
	s_addc_u32 s13, s35, 0
	s_mov_b32 s26, 1
	s_mov_b64 s[16:17], 0
	s_branch .LBB0_1431

; __device__ __forceinline__ unsigned xb_ld(unsigned* p)              { return __hip_atomic_load(p, __ATOMIC_RELAXED, __HIP_MEMORY_SCOPE_AGENT); }
; __device__ __forceinline__ unsigned xb_add(unsigned* p, unsigned v) { return __hip_atomic_fetch_add(p, v, __ATOMIC_RELAXED, __HIP_MEMORY_SCOPE_AGENT); }
; #define XB_SPIN(cond, bar) do { unsigned _sp = 0; while (cond) { __builtin_amdgcn_s_sleep(1); \
;     if ((++_sp & 255u) == 0u) { if (xb_ld(&(bar)[XB_TMO])) break; if (_sp > XB_SPIN_CAP) { atomicAdd(&(bar)[XB_TMO], 1u); break; } } } } while (0)
; __device__ __forceinline__ void xcd_barrier(const XcdBarrier& b) {
;     ...
;             const unsigned tg = og / nx;
;             if (og + 1u == (tg + 1u) * nx) xb_add(&bar[XB_TOPGEN], 1u);
;             else XB_SPIN(xb_ld(&bar[XB_TOPGEN]) == tg, bar);
.LBB0_1435:
	global_load_dword v2, v195, s[14:15] sc1
	s_add_i32 s26, s26, 1
	s_mov_b64 s[22:23], -1
	s_waitcnt vmcnt(0)
	v_cmp_ge_u32_e32 vcc, v2, v1
	s_orn2_b64 s[20:21], vcc, exec
	s_branch .LBB0_1430

; __device__ __forceinline__ unsigned xb_ld(unsigned* p)              { return __hip_atomic_load(p, __ATOMIC_RELAXED, __HIP_MEMORY_SCOPE_AGENT); }
; __device__ __forceinline__ unsigned xb_add(unsigned* p, unsigned v) { return __hip_atomic_fetch_add(p, v, __ATOMIC_RELAXED, __HIP_MEMORY_SCOPE_AGENT); }
; #define XB_SPIN(cond, bar) do { unsigned _sp = 0; while (cond) { __builtin_amdgcn_s_sleep(1); \
;     if ((++_sp & 255u) == 0u) { if (xb_ld(&(bar)[XB_TMO])) break; if (_sp > XB_SPIN_CAP) { atomicAdd(&(bar)[XB_TMO], 1u); break; } } } } while (0)
; __device__ __forceinline__ void xcd_barrier(const XcdBarrier& b) {
;     ...
;             const unsigned og = xb_add(&bar[XB_TOP], 1u);
;             const unsigned tg = og / nx;
;             if (og + 1u == (tg + 1u) * nx) xb_add(&bar[XB_TOPGEN], 1u);
;             else XB_SPIN(xb_ld(&bar[XB_TOPGEN]) == tg, bar);
.LBB0_1444:
	s_or_b64 exec, exec, s[10:11]
	s_waitcnt vmcnt(0)
	v_readfirstlane_b32 s8, v3
	v_sub_u32_e32 v4, 0, v2
	s_mov_b64 s[12:13], -1
	v_add_u32_e32 v3, s8, v1
	v_cvt_f32_u32_e32 v1, v2
	s_add_u32 s8, s34, 0x7400
	s_addc_u32 s9, s35, 0
	v_rcp_iflag_f32_e32 v1, v1
	s_nop 0
	v_mul_f32_e32 v1, 0x4f7ffffe, v1
	v_cvt_u32_f32_e32 v1, v1
	v_mul_lo_u32 v4, v4, v1
	v_mul_hi_u32 v4, v1, v4
	v_add_u32_e32 v1, v1, v4
	v_mul_hi_u32 v1, v3, v1
	v_mul_lo_u32 v4, v1, v2
	v_sub_u32_e32 v4, v3, v4
	v_cmp_ge_u32_e32 vcc, v4, v2
	v_add_u32_e32 v5, 1, v1
	v_add_u32_e32 v3, 1, v3
	v_cndmask_b32_e32 v1, v1, v5, vcc
	v_sub_u32_e32 v5, v4, v2
	v_cndmask_b32_e32 v4, v4, v5, vcc
	v_cmp_ge_u32_e32 vcc, v4, v2
	v_add_u32_e32 v4, 1, v1
	s_nop 0
	v_cndmask_b32_e32 v1, v1, v4, vcc
	v_mul_lo_u32 v4, v2, v1
	v_add_u32_e32 v2, v4, v2
	v_cmp_ne_u32_e32 vcc, v3, v2
	v_mov_b32_e32 v1, v2
	v_mov_b64_e32 v[2:3], s[8:9]
	s_and_saveexec_b64 s[10:11], vcc
	s_cbranch_execz .LBB0_1456
	global_load_dword v2, v195, s[8:9] sc1
	s_mov_b64 s[16:17], 0
	s_waitcnt vmcnt(0)
	v_cmp_gt_u32_e32 vcc, v1, v2
	s_and_saveexec_b64 s[14:15], vcc
	s_cbranch_execz .LBB0_1455
	s_add_u32 s12, s34, 0x4200
	s_addc_u32 s13, s35, 0
	s_mov_b32 s26, 1
	s_branch .LBB0_1448

; __device__ __forceinline__ unsigned xb_ld(unsigned* p)              { return __hip_atomic_load(p, __ATOMIC_RELAXED, __HIP_MEMORY_SCOPE_AGENT); }
; __device__ __forceinline__ unsigned xb_add(unsigned* p, unsigned v) { return __hip_atomic_fetch_add(p, v, __ATOMIC_RELAXED, __HIP_MEMORY_SCOPE_AGENT); }
; #define XB_SPIN(cond, bar) do { unsigned _sp = 0; while (cond) { __builtin_amdgcn_s_sleep(1); \
;     if ((++_sp & 255u) == 0u) { if (xb_ld(&(bar)[XB_TMO])) break; if (_sp > XB_SPIN_CAP) { atomicAdd(&(bar)[XB_TMO], 1u); break; } } } } while (0)
; __device__ __forceinline__ void xcd_barrier(const XcdBarrier& b) {
;     ...
;             const unsigned tg = og / nx;
;             if (og + 1u == (tg + 1u) * nx) xb_add(&bar[XB_TOPGEN], 1u);
;             else XB_SPIN(xb_ld(&bar[XB_TOPGEN]) == tg, bar);
.LBB0_1452:
	global_load_dword v2, v195, s[8:9] sc1
	s_add_i32 s26, s26, 1
	s_mov_b64 s[22:23], -1
	s_waitcnt vmcnt(0)
	v_cmp_ge_u32_e32 vcc, v2, v1
	s_orn2_b64 s[20:21], vcc, exec
	s_branch .LBB0_1447

; __device__ __forceinline__ unsigned xb_ld(unsigned* p)              { return __hip_atomic_load(p, __ATOMIC_RELAXED, __HIP_MEMORY_SCOPE_AGENT); }
; __device__ __forceinline__ unsigned xb_add(unsigned* p, unsigned v) { return __hip_atomic_fetch_add(p, v, __ATOMIC_RELAXED, __HIP_MEMORY_SCOPE_AGENT); }
; #define XB_SPIN(cond, bar) do { unsigned _sp = 0; while (cond) { __builtin_amdgcn_s_sleep(1); \
;     if ((++_sp & 255u) == 0u) { if (xb_ld(&(bar)[XB_TMO])) break; if (_sp > XB_SPIN_CAP) { atomicAdd(&(bar)[XB_TMO], 1u); break; } } } } while (0)
; __device__ __forceinline__ void xcd_barrier(const XcdBarrier& b) {
;     ...
;             if (og + 1u == (tg + 1u) * nx) xb_add(&bar[XB_TOPGEN], 1u);
;             else XB_SPIN(xb_ld(&bar[XB_TOPGEN]) == tg, bar);
;             __builtin_amdgcn_fence(__ATOMIC_ACQUIRE, "agent");
;             xb_add(&bar[XB_XGEN(b.x)], 1u);
.LBB0_1456:
	s_or_b64 exec, exec, s[10:11]
	s_and_saveexec_b64 s[8:9], s[12:13]
	s_cbranch_execz .LBB0_1458
.LBB0_1458:
	s_or_b64 exec, exec, s[8:9]
	s_mov_b64 s[8:9], exec
	v_mbcnt_lo_u32_b32 v1, s8, 0
	v_mbcnt_hi_u32_b32 v1, s9, v1
	v_cmp_eq_u32_e32 vcc, 0, v1
	s_waitcnt vmcnt(0)
	buffer_inv sc1
	s_and_saveexec_b64 s[10:11], vcc
	s_cbranch_execz .LBB0_1460
	s_bcnt1_i32_b64 s8, s[8:9]
	v_mov_b32_e32 v1, s8
	v_mov_b32_e32 v2, 0x2000

; __device__ __forceinline__ unsigned xb_ld(unsigned* p)              { return __hip_atomic_load(p, __ATOMIC_RELAXED, __HIP_MEMORY_SCOPE_AGENT); }
; __device__ __forceinline__ unsigned xb_add(unsigned* p, unsigned v) { return __hip_atomic_fetch_add(p, v, __ATOMIC_RELAXED, __HIP_MEMORY_SCOPE_AGENT); }
; #define XB_SPIN(cond, bar) do { unsigned _sp = 0; while (cond) { __builtin_amdgcn_s_sleep(1); \
;     if ((++_sp & 255u) == 0u) { if (xb_ld(&(bar)[XB_TMO])) break; if (_sp > XB_SPIN_CAP) { atomicAdd(&(bar)[XB_TMO], 1u); break; } } } } while (0)
; __device__ __forceinline__ void xcd_barrier(const XcdBarrier& b) {
;     ...
;             if (og + 1u == (tg + 1u) * nx) xb_add(&bar[XB_TOPGEN], 1u);
;             else XB_SPIN(xb_ld(&bar[XB_TOPGEN]) == tg, bar);
;             __builtin_amdgcn_fence(__ATOMIC_ACQUIRE, "agent");
;             xb_add(&bar[XB_XGEN(b.x)], 1u);
.LBB0_1532:
	s_or_b64 exec, exec, s[10:11]
	s_and_saveexec_b64 s[8:9], s[12:13]
	s_cbranch_execz .LBB0_1534
.LBB0_1534:
	s_or_b64 exec, exec, s[8:9]
	s_mov_b64 s[8:9], exec
	v_mbcnt_lo_u32_b32 v1, s8, 0
	v_mbcnt_hi_u32_b32 v1, s9, v1
	v_cmp_eq_u32_e32 vcc, 0, v1
	s_waitcnt vmcnt(0)
	buffer_inv sc1
	s_and_saveexec_b64 s[10:11], vcc
	s_cbranch_execnz .LBB0_1535
	s_getpc_b64 s[98:99]
